# P4a (attention-out projection) epilogue: 16 gate loads hoisted to epilogue start with counted vmcnt waits; fp8 GEMM first half-trip peeled (C=0) in P1/P5/P8/P9
# speedup vs baseline: 1.0096x; 1.0094x over previous
.LBB0_357:
	s_and_b64 s[10:11], s[72:73], exec
	s_cselect_b32 s5, s69, s7
	s_cselect_b32 s30, s68, s6
	s_cselect_b32 s31, s71, s9
	s_cselect_b32 s36, s70, s8
	s_add_u32 s6, s6, 0x40080
	s_addc_u32 s7, s7, 0
	s_add_u32 s37, s8, 0x100
	s_addc_u32 s67, s9, 0
	s_mov_b32 s74, -2
	ds_read_b128 v[16:19], v183
	ds_read_b128 v[20:23], v183 offset:1024
	ds_read_b128 v[24:27], v183 offset:2048
	ds_read_b128 v[28:31], v183 offset:3072
	ds_read_b128 v[0:3], v184
	ds_read_b128 v[4:7], v184 offset:1024
	ds_read_b128 v[8:11], v184 offset:2048
	ds_read_b128 v[12:15], v184 offset:3072
	s_add_u32 s8, s6, 0xfffc0080
	s_addc_u32 s9, s7, -1
	s_cmp_eq_u32 s74, 12
	s_cselect_b32 s11, s5, s9
	s_cselect_b32 s10, s30, s8
	s_cselect_b32 s9, s31, s67
	s_cselect_b32 s8, s36, s37
	v_lshl_add_u64 v[212:213], s[6:7], 0, v[170:171]
	s_add_i32 m0, s83, 0xc000
	ds_read_b128 v[174:177], v185
	ds_read_b128 v[178:181], v185 offset:1024
	ds_read_b128 v[188:191], v185 offset:2048
	ds_read_b128 v[192:195], v185 offset:3072
	ds_read_b128 v[196:199], v185 offset:4096
	ds_read_b128 v[200:203], v185 offset:5120
	ds_read_b128 v[204:207], v185 offset:6144
	ds_read_b128 v[208:211], v185 offset:7168
	global_load_lds_dwordx4 v[212:213], off
	v_lshl_add_u64 v[212:213], s[6:7], 0, v[172:173]
	s_add_i32 m0, s83, 0xe000
	s_nop 0
	global_load_lds_dwordx4 v[212:213], off
	s_waitcnt vmcnt(8)
	s_waitcnt lgkmcnt(0)
	s_barrier
	s_setprio 1
	s_waitcnt lgkmcnt(0)
	v_mfma_f32_16x16x128_f8f6f4 v[156:159], v[16:23], v[174:181], 0
	v_mfma_f32_16x16x128_f8f6f4 v[152:155], v[24:31], v[174:181], 0
	v_mfma_f32_16x16x128_f8f6f4 v[140:143], v[16:23], v[188:195], 0
	v_mfma_f32_16x16x128_f8f6f4 v[136:139], v[24:31], v[188:195], 0
	v_mfma_f32_16x16x128_f8f6f4 v[124:127], v[16:23], v[196:203], 0
	v_mfma_f32_16x16x128_f8f6f4 v[120:123], v[24:31], v[196:203], 0
	v_mfma_f32_16x16x128_f8f6f4 v[108:111], v[16:23], v[204:211], 0
	v_mfma_f32_16x16x128_f8f6f4 v[104:107], v[24:31], v[204:211], 0
	s_setprio 0
	s_setprio 1
	v_mfma_f32_16x16x128_f8f6f4 v[148:151], v[0:7], v[174:181], 0
	v_mfma_f32_16x16x128_f8f6f4 v[144:147], v[8:15], v[174:181], 0
	v_mfma_f32_16x16x128_f8f6f4 v[132:135], v[0:7], v[188:195], 0
	v_mfma_f32_16x16x128_f8f6f4 v[128:131], v[8:15], v[188:195], 0
	v_mfma_f32_16x16x128_f8f6f4 v[116:119], v[0:7], v[196:203], 0
	v_mfma_f32_16x16x128_f8f6f4 v[112:115], v[8:15], v[196:203], 0
	v_mfma_f32_16x16x128_f8f6f4 v[100:103], v[0:7], v[204:211], 0
	v_mfma_f32_16x16x128_f8f6f4 v[96:99], v[8:15], v[204:211], 0
	s_setprio 0
	s_barrier
	s_add_i32 s75, s89, s38
	v_lshl_add_u64 v[174:175], s[8:9], 0, v[162:163]
	s_mov_b32 m0, s75
	ds_read_b128 v[188:191], v185 offset:16384
	ds_read_b128 v[192:195], v185 offset:17408
	ds_read_b128 v[196:199], v185 offset:18432
	ds_read_b128 v[200:203], v185 offset:19456
	ds_read_b128 v[204:207], v185 offset:20480
	ds_read_b128 v[208:211], v185 offset:21504
	ds_read_b128 v[212:215], v185 offset:22528
	ds_read_b128 v[216:219], v185 offset:23552
	global_load_lds_dwordx4 v[174:175], off
	s_add_i32 m0, s75, 0x2000
	s_add_u32 s76, s8, 0x40000
	v_lshl_add_u64 v[176:177], s[8:9], 0, v[166:167]
	s_addc_u32 s77, s9, 0
	s_add_i32 s75, s90, s38
	global_load_lds_dwordx4 v[176:177], off
	v_lshl_add_u64 v[178:179], s[76:77], 0, v[162:163]
	s_mov_b32 m0, s75
	v_lshl_add_u64 v[180:181], s[10:11], 0, v[164:165]
	global_load_lds_dwordx4 v[178:179], off
	v_lshl_add_u64 v[178:179], s[76:77], 0, v[166:167]
	s_add_i32 m0, s75, 0x2000
	s_nop 0
	global_load_lds_dwordx4 v[178:179], off
	v_lshl_add_u64 v[178:179], s[10:11], 0, v[160:161]
	s_mov_b32 m0, s83
	s_nop 0
	global_load_lds_dwordx4 v[178:179], off
	s_mov_b32 m0, s84
	s_nop 0
	global_load_lds_dwordx4 v[180:181], off
	s_waitcnt vmcnt(8)
	s_waitcnt lgkmcnt(0)
	s_barrier
	s_setprio 1
	s_waitcnt lgkmcnt(0)
	v_mfma_f32_16x16x128_f8f6f4 v[92:95], v[16:23], v[188:195], 0
	v_mfma_f32_16x16x128_f8f6f4 v[88:91], v[24:31], v[188:195], 0
	v_mfma_f32_16x16x128_f8f6f4 v[76:79], v[16:23], v[196:203], 0
	v_mfma_f32_16x16x128_f8f6f4 v[72:75], v[24:31], v[196:203], 0
	v_mfma_f32_16x16x128_f8f6f4 v[60:63], v[16:23], v[204:211], 0
	v_mfma_f32_16x16x128_f8f6f4 v[56:59], v[24:31], v[204:211], 0
	v_mfma_f32_16x16x128_f8f6f4 v[44:47], v[16:23], v[212:219], 0
	v_mfma_f32_16x16x128_f8f6f4 v[40:43], v[24:31], v[212:219], 0
	s_setprio 0
	s_setprio 1
	v_mfma_f32_16x16x128_f8f6f4 v[84:87], v[0:7], v[188:195], 0
	v_mfma_f32_16x16x128_f8f6f4 v[80:83], v[8:15], v[188:195], 0
	v_mfma_f32_16x16x128_f8f6f4 v[68:71], v[0:7], v[196:203], 0
	v_mfma_f32_16x16x128_f8f6f4 v[64:67], v[8:15], v[196:203], 0
	v_mfma_f32_16x16x128_f8f6f4 v[52:55], v[0:7], v[204:211], 0
	v_mfma_f32_16x16x128_f8f6f4 v[48:51], v[8:15], v[204:211], 0
	v_mfma_f32_16x16x128_f8f6f4 v[36:39], v[0:7], v[212:219], 0
	v_mfma_f32_16x16x128_f8f6f4 v[32:35], v[8:15], v[212:219], 0
	s_setprio 0
	s_barrier
	s_branch .Lpeel1f_sub3

.Lpeel1f_sub3:
	s_add_i32 s75, 0, 0x18000
	s_add_i32 s76, 0, 0x1c000
	v_add_u32_e32 v12, s75, v182
	v_add_u32_e32 v28, s76, v182
	ds_read_b128 v[0:3], v12
	ds_read_b128 v[4:7], v12 offset:1024
	ds_read_b128 v[8:11], v12 offset:2048
	ds_read_b128 v[12:15], v12 offset:3072
	ds_read_b128 v[16:19], v28
	ds_read_b128 v[20:23], v28 offset:1024
	ds_read_b128 v[24:27], v28 offset:2048
	ds_read_b128 v[28:31], v28 offset:3072
	s_add_u32 s10, s10, 0x40000
	s_addc_u32 s11, s11, 0
	s_mov_b32 m0, s85
	v_lshl_add_u64 v[220:221], s[10:11], 0, v[160:161]
	ds_read_b128 v[188:191], v185 offset:32768
	ds_read_b128 v[192:195], v185 offset:33792
	ds_read_b128 v[196:199], v185 offset:34816
	ds_read_b128 v[200:203], v185 offset:35840
	ds_read_b128 v[204:207], v185 offset:36864
	ds_read_b128 v[208:211], v185 offset:37888
	ds_read_b128 v[212:215], v185 offset:38912
	ds_read_b128 v[216:219], v185 offset:39936
	global_load_lds_dwordx4 v[220:221], off
	v_lshl_add_u64 v[220:221], s[10:11], 0, v[164:165]
	s_mov_b32 m0, s86
	s_nop 0
	global_load_lds_dwordx4 v[220:221], off
	s_waitcnt vmcnt(8)
	s_waitcnt lgkmcnt(0)
	s_barrier
	s_setprio 1
	s_waitcnt lgkmcnt(0)
	v_mfma_f32_16x16x128_f8f6f4 v[156:159], v[0:7], v[188:195], v[156:159]
	v_mfma_f32_16x16x128_f8f6f4 v[152:155], v[8:15], v[188:195], v[152:155]
	v_mfma_f32_16x16x128_f8f6f4 v[140:143], v[0:7], v[196:203], v[140:143]
	v_mfma_f32_16x16x128_f8f6f4 v[136:139], v[8:15], v[196:203], v[136:139]
	v_mfma_f32_16x16x128_f8f6f4 v[124:127], v[0:7], v[204:211], v[124:127]
	v_mfma_f32_16x16x128_f8f6f4 v[120:123], v[8:15], v[204:211], v[120:123]
	v_mfma_f32_16x16x128_f8f6f4 v[108:111], v[0:7], v[212:219], v[108:111]
	v_mfma_f32_16x16x128_f8f6f4 v[104:107], v[8:15], v[212:219], v[104:107]
	s_setprio 0
	s_setprio 1
	v_mfma_f32_16x16x128_f8f6f4 v[148:151], v[16:23], v[188:195], v[148:151]
	v_mfma_f32_16x16x128_f8f6f4 v[144:147], v[24:31], v[188:195], v[144:147]
	v_mfma_f32_16x16x128_f8f6f4 v[132:135], v[16:23], v[196:203], v[132:135]
	v_mfma_f32_16x16x128_f8f6f4 v[128:131], v[24:31], v[196:203], v[128:131]
	v_mfma_f32_16x16x128_f8f6f4 v[116:119], v[16:23], v[204:211], v[116:119]
	v_mfma_f32_16x16x128_f8f6f4 v[112:115], v[24:31], v[204:211], v[112:115]
	v_mfma_f32_16x16x128_f8f6f4 v[100:103], v[16:23], v[212:219], v[100:103]
	v_mfma_f32_16x16x128_f8f6f4 v[96:99], v[24:31], v[212:219], v[96:99]
	s_setprio 0
	s_barrier
	s_add_i32 s10, s75, s38
	v_lshl_add_u64 v[174:175], v[174:175], 0, s[42:43]
	s_mov_b32 m0, s10
	ds_read_b128 v[188:191], v185 offset:49152
	ds_read_b128 v[192:195], v185 offset:50176
	ds_read_b128 v[196:199], v185 offset:51200
	ds_read_b128 v[200:203], v185 offset:52224
	ds_read_b128 v[204:207], v185 offset:53248
	ds_read_b128 v[208:211], v185 offset:54272
	ds_read_b128 v[212:215], v185 offset:55296
	ds_read_b128 v[216:219], v185 offset:56320
	global_load_lds_dwordx4 v[174:175], off
	s_add_i32 m0, s10, 0x2000
	s_add_u32 s8, s8, 0x40080
	v_lshl_add_u64 v[174:175], v[176:177], 0, s[42:43]
	s_addc_u32 s9, s9, 0
	s_add_i32 s10, s76, s38
	global_load_lds_dwordx4 v[174:175], off
	v_lshl_add_u64 v[174:175], s[8:9], 0, v[162:163]
	s_mov_b32 m0, s10
	s_nop 0
	global_load_lds_dwordx4 v[174:175], off
	v_lshl_add_u64 v[174:175], s[8:9], 0, v[166:167]
	s_add_i32 m0, s10, 0x2000
	s_nop 0
	global_load_lds_dwordx4 v[174:175], off
	v_lshl_add_u64 v[174:175], v[178:179], 0, s[42:43]
	s_mov_b32 m0, s87
	s_nop 0
	global_load_lds_dwordx4 v[174:175], off
	v_lshl_add_u64 v[174:175], v[180:181], 0, s[42:43]
	s_mov_b32 m0, s88
	s_nop 0
	global_load_lds_dwordx4 v[174:175], off
	s_waitcnt vmcnt(8)
	s_waitcnt lgkmcnt(0)
	s_barrier
	s_setprio 1
	s_waitcnt lgkmcnt(0)
	v_mfma_f32_16x16x128_f8f6f4 v[92:95], v[0:7], v[188:195], v[92:95]
	v_mfma_f32_16x16x128_f8f6f4 v[88:91], v[8:15], v[188:195], v[88:91]
	v_mfma_f32_16x16x128_f8f6f4 v[76:79], v[0:7], v[196:203], v[76:79]
	v_mfma_f32_16x16x128_f8f6f4 v[72:75], v[8:15], v[196:203], v[72:75]
	v_mfma_f32_16x16x128_f8f6f4 v[60:63], v[0:7], v[204:211], v[60:63]
	v_mfma_f32_16x16x128_f8f6f4 v[56:59], v[8:15], v[204:211], v[56:59]
	v_mfma_f32_16x16x128_f8f6f4 v[44:47], v[0:7], v[212:219], v[44:47]
	v_mfma_f32_16x16x128_f8f6f4 v[40:43], v[8:15], v[212:219], v[40:43]
	s_setprio 0
	s_setprio 1
	v_mfma_f32_16x16x128_f8f6f4 v[84:87], v[16:23], v[188:195], v[84:87]
	v_mfma_f32_16x16x128_f8f6f4 v[80:83], v[24:31], v[188:195], v[80:83]
	v_mfma_f32_16x16x128_f8f6f4 v[68:71], v[16:23], v[196:203], v[68:71]
	v_mfma_f32_16x16x128_f8f6f4 v[64:67], v[24:31], v[196:203], v[64:67]
	v_mfma_f32_16x16x128_f8f6f4 v[52:55], v[16:23], v[204:211], v[52:55]
	v_mfma_f32_16x16x128_f8f6f4 v[48:51], v[24:31], v[204:211], v[48:51]
	v_mfma_f32_16x16x128_f8f6f4 v[36:39], v[16:23], v[212:219], v[36:39]
	v_mfma_f32_16x16x128_f8f6f4 v[32:35], v[24:31], v[212:219], v[32:35]
	s_setprio 0
	s_barrier
	s_add_i32 s74, s74, 2
	s_add_u32 s6, s6, 0x100
	s_addc_u32 s7, s7, 0
	s_add_u32 s37, s37, 0x100
	s_addc_u32 s67, s67, 0
	s_cmp_gt_u32 s74, 13
	s_cbranch_scc0 .LBB0_358
	s_and_b64 vcc, exec, s[44:45]
	s_cbranch_vccz .LBB0_361
	s_barrier

.LBB0_860:
	s_lshl_b32 s25, s40, 8
	v_mbcnt_lo_u32_b32 v144, -1, 0
	v_mbcnt_hi_u32_b32 v144, -1, v144
	s_add_i32 s25, s25, s39
	v_and_or_b32 v148, v144, 15, s25
	s_lshl_b32 s25, s57, 8
	v_ashrrev_i32_e32 v144, 1, v144
	s_or_b32 s25, s25, s46
	v_and_b32_e32 v144, -8, v144
	v_add_u32_e32 v144, s25, v144
	v_ashrrev_i32_e32 v149, 31, v148
	v_lshlrev_b64 v[146:147], 13, v[148:149]
	v_ashrrev_i32_e32 v145, 31, v144
	v_lshl_add_u64 v[150:151], s[8:9], 0, v[146:147]
	v_lshlrev_b64 v[146:147], 1, v[144:145]
	v_lshl_add_u64 v[150:151], v[150:151], 0, v[146:147]
	s_mov_b32 s98, 0x20000
	s_mov_b32 s99, 0
	global_load_dwordx4 v[168:171], v[150:151], off
	global_load_dwordx4 v[172:175], v[150:151], off offset:256
	v_lshl_add_u64 v[232:233], v[150:151], 0, s[98:99]
	global_load_dwordx4 v[176:179], v[232:233], off
	global_load_dwordx4 v[180:183], v[232:233], off offset:256
	v_lshl_add_u64 v[232:233], v[232:233], 0, s[98:99]
	global_load_dwordx4 v[184:187], v[232:233], off
	global_load_dwordx4 v[188:191], v[232:233], off offset:256
	v_lshl_add_u64 v[232:233], v[232:233], 0, s[98:99]
	global_load_dwordx4 v[192:195], v[232:233], off
	global_load_dwordx4 v[196:199], v[232:233], off offset:256
	v_lshl_add_u64 v[232:233], v[232:233], 0, s[98:99]
	v_lshl_add_u64 v[232:233], v[232:233], 0, s[98:99]
	v_lshl_add_u64 v[232:233], v[232:233], 0, s[98:99]
	v_lshl_add_u64 v[232:233], v[232:233], 0, s[98:99]
	v_lshl_add_u64 v[232:233], v[232:233], 0, s[98:99]
	global_load_dwordx4 v[200:203], v[232:233], off
	global_load_dwordx4 v[204:207], v[232:233], off offset:256
	v_lshl_add_u64 v[232:233], v[232:233], 0, s[98:99]
	global_load_dwordx4 v[208:211], v[232:233], off
	global_load_dwordx4 v[212:215], v[232:233], off offset:256
	v_lshl_add_u64 v[232:233], v[232:233], 0, s[98:99]
	global_load_dwordx4 v[216:219], v[232:233], off
	global_load_dwordx4 v[220:223], v[232:233], off offset:256
	v_lshl_add_u64 v[232:233], v[232:233], 0, s[98:99]
	global_load_dwordx4 v[224:227], v[232:233], off
	global_load_dwordx4 v[228:231], v[232:233], off offset:256
	v_pk_mul_f32 v[128:129], v[128:129], s[22:23] op_sel_hi:[1,0]
	v_pk_mul_f32 v[124:125], v[124:125], s[22:23] op_sel_hi:[1,0]
	v_mov_b32_e32 v162, 0
	v_mov_b32_e32 v163, 0
	v_pk_mul_f32 v[130:131], v[130:131], s[22:23] op_sel_hi:[1,0]
	v_pk_mul_f32 v[126:127], v[126:127], s[22:23] op_sel_hi:[1,0]
	v_pk_mul_f32 v[120:121], v[120:121], s[22:23] op_sel_hi:[1,0]
	v_pk_mul_f32 v[116:117], v[116:117], s[22:23] op_sel_hi:[1,0]
	v_pk_mul_f32 v[122:123], v[122:123], s[22:23] op_sel_hi:[1,0]
	v_pk_mul_f32 v[118:119], v[118:119], s[22:23] op_sel_hi:[1,0]
	v_pk_mul_f32 v[112:113], v[112:113], s[22:23] op_sel_hi:[1,0]
	v_pk_mul_f32 v[108:109], v[108:109], s[22:23] op_sel_hi:[1,0]
	v_pk_mul_f32 v[114:115], v[114:115], s[22:23] op_sel_hi:[1,0]
	v_pk_mul_f32 v[110:111], v[110:111], s[22:23] op_sel_hi:[1,0]
	v_pk_mul_f32 v[104:105], v[104:105], s[22:23] op_sel_hi:[1,0]
	v_pk_mul_f32 v[100:101], v[100:101], s[22:23] op_sel_hi:[1,0]
	v_pk_mul_f32 v[106:107], v[106:107], s[22:23] op_sel_hi:[1,0]
	v_pk_mul_f32 v[102:103], v[102:103], s[22:23] op_sel_hi:[1,0]
	v_pk_mul_f32 v[96:97], v[96:97], s[22:23] op_sel_hi:[1,0]
	v_pk_mul_f32 v[92:93], v[92:93], s[22:23] op_sel_hi:[1,0]
	v_pk_mul_f32 v[98:99], v[98:99], s[22:23] op_sel_hi:[1,0]
	v_pk_mul_f32 v[94:95], v[94:95], s[22:23] op_sel_hi:[1,0]
	v_pk_mul_f32 v[88:89], v[88:89], s[22:23] op_sel_hi:[1,0]
	v_pk_mul_f32 v[84:85], v[84:85], s[22:23] op_sel_hi:[1,0]
	v_pk_mul_f32 v[90:91], v[90:91], s[22:23] op_sel_hi:[1,0]
	v_pk_mul_f32 v[86:87], v[86:87], s[22:23] op_sel_hi:[1,0]
	v_pk_mul_f32 v[80:81], v[80:81], s[22:23] op_sel_hi:[1,0]
	v_pk_mul_f32 v[76:77], v[76:77], s[22:23] op_sel_hi:[1,0]
	v_pk_mul_f32 v[82:83], v[82:83], s[22:23] op_sel_hi:[1,0]
	v_pk_mul_f32 v[78:79], v[78:79], s[22:23] op_sel_hi:[1,0]
	v_pk_mul_f32 v[72:73], v[72:73], s[22:23] op_sel_hi:[1,0]
	v_pk_mul_f32 v[68:69], v[68:69], s[22:23] op_sel_hi:[1,0]
	v_pk_mul_f32 v[74:75], v[74:75], s[22:23] op_sel_hi:[1,0]
	v_pk_mul_f32 v[70:71], v[70:71], s[22:23] op_sel_hi:[1,0]
	v_pk_mul_f32 v[64:65], v[64:65], s[22:23] op_sel_hi:[1,0]
	v_pk_mul_f32 v[60:61], v[60:61], s[22:23] op_sel_hi:[1,0]
	v_pk_mul_f32 v[66:67], v[66:67], s[22:23] op_sel_hi:[1,0]
	v_pk_mul_f32 v[62:63], v[62:63], s[22:23] op_sel_hi:[1,0]
	v_pk_mul_f32 v[56:57], v[56:57], s[22:23] op_sel_hi:[1,0]
	v_pk_mul_f32 v[52:53], v[52:53], s[22:23] op_sel_hi:[1,0]
	v_pk_mul_f32 v[58:59], v[58:59], s[22:23] op_sel_hi:[1,0]
	v_pk_mul_f32 v[54:55], v[54:55], s[22:23] op_sel_hi:[1,0]
	v_pk_mul_f32 v[48:49], v[48:49], s[22:23] op_sel_hi:[1,0]
	v_pk_mul_f32 v[44:45], v[44:45], s[22:23] op_sel_hi:[1,0]
	v_pk_mul_f32 v[50:51], v[50:51], s[22:23] op_sel_hi:[1,0]
	v_pk_mul_f32 v[46:47], v[46:47], s[22:23] op_sel_hi:[1,0]
	v_pk_mul_f32 v[40:41], v[40:41], s[22:23] op_sel_hi:[1,0]
	v_pk_mul_f32 v[36:37], v[36:37], s[22:23] op_sel_hi:[1,0]
	v_pk_mul_f32 v[42:43], v[42:43], s[22:23] op_sel_hi:[1,0]
	v_pk_mul_f32 v[38:39], v[38:39], s[22:23] op_sel_hi:[1,0]
	v_pk_mul_f32 v[32:33], v[32:33], s[22:23] op_sel_hi:[1,0]
	v_pk_mul_f32 v[28:29], v[28:29], s[22:23] op_sel_hi:[1,0]
	v_pk_mul_f32 v[34:35], v[34:35], s[22:23] op_sel_hi:[1,0]
	v_pk_mul_f32 v[30:31], v[30:31], s[22:23] op_sel_hi:[1,0]
	v_pk_mul_f32 v[24:25], v[24:25], s[22:23] op_sel_hi:[1,0]
	v_pk_mul_f32 v[20:21], v[20:21], s[22:23] op_sel_hi:[1,0]
	v_pk_mul_f32 v[26:27], v[26:27], s[22:23] op_sel_hi:[1,0]
	v_pk_mul_f32 v[22:23], v[22:23], s[22:23] op_sel_hi:[1,0]
	v_pk_mul_f32 v[16:17], v[16:17], s[22:23] op_sel_hi:[1,0]
	v_pk_mul_f32 v[12:13], v[12:13], s[22:23] op_sel_hi:[1,0]
	v_pk_mul_f32 v[18:19], v[18:19], s[22:23] op_sel_hi:[1,0]
	v_pk_mul_f32 v[14:15], v[14:15], s[22:23] op_sel_hi:[1,0]
	v_pk_mul_f32 v[8:9], v[8:9], s[22:23] op_sel_hi:[1,0]
	v_pk_mul_f32 v[4:5], v[4:5], s[22:23] op_sel_hi:[1,0]
	v_pk_mul_f32 v[10:11], v[10:11], s[22:23] op_sel_hi:[1,0]
	v_pk_mul_f32 v[6:7], v[6:7], s[22:23] op_sel_hi:[1,0]
	s_andn2_b64 vcc, exec, s[0:1]
	s_mov_b64 s[0:1], -1
	s_waitcnt vmcnt(15)
	v_lshlrev_b32_e32 v157, 16, v168
	v_and_b32_e32 v158, 0xffff0000, v168
	v_lshlrev_b32_e32 v165, 16, v170
	v_and_b32_e32 v160, 0xffff0000, v170
	v_mul_f32_e32 v128, v128, v157
	v_mul_f32_e32 v129, v129, v158
	v_mul_f32_e32 v124, v124, v165
	v_mul_f32_e32 v125, v125, v160
	v_mul_f32_e32 v128, 0x41800000, v128
	v_mul_f32_e32 v129, 0x41800000, v129
	v_mul_f32_e32 v124, 0x41800000, v124
	v_mul_f32_e32 v125, 0x41800000, v125
	v_med3_f32 v128, v128, s56, v156
	v_med3_f32 v129, v129, s56, v156
	v_med3_f32 v124, v124, s56, v156
	v_med3_f32 v125, v125, s56, v156
	v_lshlrev_b32_e32 v164, 16, v169
	v_and_b32_e32 v159, 0xffff0000, v169
	v_lshlrev_b32_e32 v166, 16, v171
	v_and_b32_e32 v161, 0xffff0000, v171
	v_cvt_pk_fp8_f32 v162, v128, v129
	v_cvt_pk_fp8_f32 v163, v124, v125
	v_mul_f32_e32 v130, v130, v164
	v_mul_f32_e32 v131, v131, v159
	v_mul_f32_e32 v126, v126, v166
	v_mul_f32_e32 v127, v127, v161
	v_mul_f32_e32 v130, 0x41800000, v130
	v_mul_f32_e32 v131, 0x41800000, v131
	v_mul_f32_e32 v126, 0x41800000, v126
	v_mul_f32_e32 v127, 0x41800000, v127
	v_med3_f32 v130, v130, s56, v156
	v_med3_f32 v131, v131, s56, v156
	v_med3_f32 v124, v126, s56, v156
	v_med3_f32 v125, v127, s56, v156
	v_cvt_pk_fp8_f32 v162, v130, v131 op_sel:[0,0,1]
	v_cvt_pk_fp8_f32 v163, v124, v125 op_sel:[0,0,1]
	v_lshlrev_b64 v[124:125], 11, v[148:149]
	v_lshl_add_u64 v[124:125], s[6:7], 0, v[124:125]
	v_lshl_add_u64 v[128:129], v[124:125], 0, v[144:145]
	global_store_dwordx2 v[128:129], v[162:163], off
	v_mov_b32_e32 v130, 0
	v_mov_b32_e32 v131, 0
	v_or_b32_e32 v150, 16, v148
	v_ashrrev_i32_e32 v151, 31, v150
	s_waitcnt vmcnt(15)
	v_lshlrev_b32_e32 v149, 16, v172
	v_and_b32_e32 v124, 0xffff0000, v172
	v_lshlrev_b32_e32 v158, 16, v174
	v_and_b32_e32 v126, 0xffff0000, v174
	v_mul_f32_e32 v120, v120, v149
	v_mul_f32_e32 v121, v121, v124
	v_mul_f32_e32 v116, v116, v158
	v_mul_f32_e32 v117, v117, v126
	v_mul_f32_e32 v120, 0x41800000, v120
	v_mul_f32_e32 v121, 0x41800000, v121
	v_mul_f32_e32 v116, 0x41800000, v116
	v_mul_f32_e32 v117, 0x41800000, v117
	v_med3_f32 v120, v120, s56, v156
	v_med3_f32 v121, v121, s56, v156
	v_med3_f32 v116, v116, s56, v156
	v_med3_f32 v117, v117, s56, v156
	v_lshlrev_b32_e32 v157, 16, v173
	v_and_b32_e32 v125, 0xffff0000, v173
	v_lshlrev_b32_e32 v159, 16, v175
	v_and_b32_e32 v127, 0xffff0000, v175
	v_cvt_pk_fp8_f32 v130, v120, v121
	v_cvt_pk_fp8_f32 v131, v116, v117
	v_mul_f32_e32 v122, v122, v157
	v_mul_f32_e32 v123, v123, v125
	v_mul_f32_e32 v118, v118, v159
	v_mul_f32_e32 v119, v119, v127
	v_mul_f32_e32 v122, 0x41800000, v122
	v_mul_f32_e32 v123, 0x41800000, v123
	v_mul_f32_e32 v118, 0x41800000, v118
	v_mul_f32_e32 v119, 0x41800000, v119
	v_med3_f32 v122, v122, s56, v156
	v_med3_f32 v123, v123, s56, v156
	v_med3_f32 v116, v118, s56, v156
	v_med3_f32 v117, v119, s56, v156
	v_cvt_pk_fp8_f32 v130, v122, v123 op_sel:[0,0,1]
	v_cvt_pk_fp8_f32 v131, v116, v117 op_sel:[0,0,1]
	v_lshlrev_b64 v[116:117], 13, v[150:151]
	v_lshl_add_u64 v[116:117], s[8:9], 0, v[116:117]
	v_lshl_add_u64 v[120:121], v[116:117], 0, v[146:147]
	global_store_dwordx2 v[128:129], v[130:131], off offset:128
	v_mov_b32_e32 v122, 0
	v_mov_b32_e32 v123, 0
	s_waitcnt vmcnt(15)
	v_lshlrev_b32_e32 v124, 16, v176
	v_and_b32_e32 v116, 0xffff0000, v176
	v_lshlrev_b32_e32 v126, 16, v178
	v_and_b32_e32 v118, 0xffff0000, v178
	v_mul_f32_e32 v112, v112, v124
	v_mul_f32_e32 v113, v113, v116
	v_mul_f32_e32 v108, v108, v126
	v_mul_f32_e32 v109, v109, v118
	v_mul_f32_e32 v112, 0x41800000, v112
	v_mul_f32_e32 v113, 0x41800000, v113
	v_mul_f32_e32 v108, 0x41800000, v108
	v_mul_f32_e32 v109, 0x41800000, v109
	v_med3_f32 v112, v112, s56, v156
	v_med3_f32 v113, v113, s56, v156
	v_med3_f32 v108, v108, s56, v156
	v_med3_f32 v109, v109, s56, v156
	v_lshlrev_b32_e32 v125, 16, v177
	v_and_b32_e32 v117, 0xffff0000, v177
	v_lshlrev_b32_e32 v127, 16, v179
	v_and_b32_e32 v119, 0xffff0000, v179
	v_cvt_pk_fp8_f32 v122, v112, v113
	v_cvt_pk_fp8_f32 v123, v108, v109
	v_mul_f32_e32 v114, v114, v125
	v_mul_f32_e32 v115, v115, v117
	v_mul_f32_e32 v110, v110, v127
	v_mul_f32_e32 v111, v111, v119
	v_mul_f32_e32 v114, 0x41800000, v114
	v_mul_f32_e32 v115, 0x41800000, v115
	v_mul_f32_e32 v110, 0x41800000, v110
	v_mul_f32_e32 v111, 0x41800000, v111
	v_med3_f32 v114, v114, s56, v156
	v_med3_f32 v115, v115, s56, v156
	v_med3_f32 v108, v110, s56, v156
	v_med3_f32 v109, v111, s56, v156
	v_cvt_pk_fp8_f32 v122, v114, v115 op_sel:[0,0,1]
	v_cvt_pk_fp8_f32 v123, v108, v109 op_sel:[0,0,1]
	v_lshlrev_b64 v[108:109], 11, v[150:151]
	v_lshl_add_u64 v[108:109], s[6:7], 0, v[108:109]
	v_lshl_add_u64 v[112:113], v[108:109], 0, v[144:145]
	global_store_dwordx2 v[112:113], v[122:123], off
	v_mov_b32_e32 v114, 0
	v_mov_b32_e32 v115, 0
	v_or_b32_e32 v116, 32, v148
	v_ashrrev_i32_e32 v117, 31, v116
	s_waitcnt vmcnt(15)
	v_lshlrev_b32_e32 v118, 16, v180
	v_and_b32_e32 v108, 0xffff0000, v180
	v_lshlrev_b32_e32 v120, 16, v182
	v_and_b32_e32 v110, 0xffff0000, v182
	v_mul_f32_e32 v104, v104, v118
	v_mul_f32_e32 v105, v105, v108
	v_mul_f32_e32 v100, v100, v120
	v_mul_f32_e32 v101, v101, v110
	v_mul_f32_e32 v104, 0x41800000, v104
	v_mul_f32_e32 v105, 0x41800000, v105
	v_mul_f32_e32 v100, 0x41800000, v100
	v_mul_f32_e32 v101, 0x41800000, v101
	v_med3_f32 v104, v104, s56, v156
	v_med3_f32 v105, v105, s56, v156
	v_med3_f32 v100, v100, s56, v156
	v_med3_f32 v101, v101, s56, v156
	v_lshlrev_b32_e32 v119, 16, v181
	v_and_b32_e32 v109, 0xffff0000, v181
	v_lshlrev_b32_e32 v121, 16, v183
	v_and_b32_e32 v111, 0xffff0000, v183
	v_cvt_pk_fp8_f32 v114, v104, v105
	v_cvt_pk_fp8_f32 v115, v100, v101
	v_mul_f32_e32 v106, v106, v119
	v_mul_f32_e32 v107, v107, v109
	v_mul_f32_e32 v102, v102, v121
	v_mul_f32_e32 v103, v103, v111
	v_mul_f32_e32 v106, 0x41800000, v106
	v_mul_f32_e32 v107, 0x41800000, v107
	v_mul_f32_e32 v102, 0x41800000, v102
	v_mul_f32_e32 v103, 0x41800000, v103
	v_med3_f32 v106, v106, s56, v156
	v_med3_f32 v107, v107, s56, v156
	v_med3_f32 v100, v102, s56, v156
	v_med3_f32 v101, v103, s56, v156
	v_cvt_pk_fp8_f32 v114, v106, v107 op_sel:[0,0,1]
	v_cvt_pk_fp8_f32 v115, v100, v101 op_sel:[0,0,1]
	v_lshlrev_b64 v[100:101], 13, v[116:117]
	v_lshl_add_u64 v[100:101], s[8:9], 0, v[100:101]
	v_lshl_add_u64 v[104:105], v[100:101], 0, v[146:147]
	global_store_dwordx2 v[112:113], v[114:115], off offset:128
	v_mov_b32_e32 v106, 0
	v_mov_b32_e32 v107, 0
	s_waitcnt vmcnt(15)
	v_lshlrev_b32_e32 v108, 16, v184
	v_and_b32_e32 v100, 0xffff0000, v184
	v_lshlrev_b32_e32 v110, 16, v186
	v_and_b32_e32 v102, 0xffff0000, v186
	v_mul_f32_e32 v96, v96, v108
	v_mul_f32_e32 v97, v97, v100
	v_mul_f32_e32 v92, v92, v110
	v_mul_f32_e32 v93, v93, v102
	v_mul_f32_e32 v96, 0x41800000, v96
	v_mul_f32_e32 v97, 0x41800000, v97
	v_mul_f32_e32 v92, 0x41800000, v92
	v_mul_f32_e32 v93, 0x41800000, v93
	v_med3_f32 v96, v96, s56, v156
	v_med3_f32 v97, v97, s56, v156
	v_med3_f32 v92, v92, s56, v156
	v_med3_f32 v93, v93, s56, v156
	v_lshlrev_b32_e32 v109, 16, v185
	v_and_b32_e32 v101, 0xffff0000, v185
	v_lshlrev_b32_e32 v111, 16, v187
	v_and_b32_e32 v103, 0xffff0000, v187
	v_cvt_pk_fp8_f32 v106, v96, v97
	v_cvt_pk_fp8_f32 v107, v92, v93
	v_mul_f32_e32 v98, v98, v109
	v_mul_f32_e32 v99, v99, v101
	v_mul_f32_e32 v94, v94, v111
	v_mul_f32_e32 v95, v95, v103
	v_mul_f32_e32 v98, 0x41800000, v98
	v_mul_f32_e32 v99, 0x41800000, v99
	v_mul_f32_e32 v94, 0x41800000, v94
	v_mul_f32_e32 v95, 0x41800000, v95
	v_med3_f32 v98, v98, s56, v156
	v_med3_f32 v99, v99, s56, v156
	v_med3_f32 v92, v94, s56, v156
	v_med3_f32 v93, v95, s56, v156
	v_cvt_pk_fp8_f32 v106, v98, v99 op_sel:[0,0,1]
	v_cvt_pk_fp8_f32 v107, v92, v93 op_sel:[0,0,1]
	v_lshlrev_b64 v[92:93], 11, v[116:117]
	v_lshl_add_u64 v[92:93], s[6:7], 0, v[92:93]
	v_lshl_add_u64 v[96:97], v[92:93], 0, v[144:145]
	global_store_dwordx2 v[96:97], v[106:107], off
	v_mov_b32_e32 v98, 0
	v_mov_b32_e32 v99, 0
	v_or_b32_e32 v100, 48, v148
	v_ashrrev_i32_e32 v101, 31, v100
	s_waitcnt vmcnt(15)
	v_lshlrev_b32_e32 v102, 16, v188
	v_and_b32_e32 v92, 0xffff0000, v188
	v_lshlrev_b32_e32 v104, 16, v190
	v_and_b32_e32 v94, 0xffff0000, v190
	v_mul_f32_e32 v88, v88, v102
	v_mul_f32_e32 v89, v89, v92
	v_mul_f32_e32 v84, v84, v104
	v_mul_f32_e32 v85, v85, v94
	v_mul_f32_e32 v88, 0x41800000, v88
	v_mul_f32_e32 v89, 0x41800000, v89
	v_mul_f32_e32 v84, 0x41800000, v84
	v_mul_f32_e32 v85, 0x41800000, v85
	v_med3_f32 v88, v88, s56, v156
	v_med3_f32 v89, v89, s56, v156
	v_med3_f32 v84, v84, s56, v156
	v_med3_f32 v85, v85, s56, v156
	v_lshlrev_b32_e32 v103, 16, v189
	v_and_b32_e32 v93, 0xffff0000, v189
	v_lshlrev_b32_e32 v105, 16, v191
	v_and_b32_e32 v95, 0xffff0000, v191
	v_cvt_pk_fp8_f32 v98, v88, v89
	v_cvt_pk_fp8_f32 v99, v84, v85
	v_mul_f32_e32 v90, v90, v103
	v_mul_f32_e32 v91, v91, v93
	v_mul_f32_e32 v86, v86, v105
	v_mul_f32_e32 v87, v87, v95
	v_mul_f32_e32 v90, 0x41800000, v90
	v_mul_f32_e32 v91, 0x41800000, v91
	v_mul_f32_e32 v86, 0x41800000, v86
	v_mul_f32_e32 v87, 0x41800000, v87
	v_med3_f32 v90, v90, s56, v156
	v_med3_f32 v91, v91, s56, v156
	v_med3_f32 v84, v86, s56, v156
	v_med3_f32 v85, v87, s56, v156
	v_cvt_pk_fp8_f32 v98, v90, v91 op_sel:[0,0,1]
	v_cvt_pk_fp8_f32 v99, v84, v85 op_sel:[0,0,1]
	v_lshlrev_b64 v[84:85], 13, v[100:101]
	v_lshl_add_u64 v[84:85], s[8:9], 0, v[84:85]
	v_lshl_add_u64 v[88:89], v[84:85], 0, v[146:147]
	global_store_dwordx2 v[96:97], v[98:99], off offset:128
	v_mov_b32_e32 v90, 0
	v_mov_b32_e32 v91, 0
	s_waitcnt vmcnt(15)
	v_lshlrev_b32_e32 v92, 16, v192
	v_and_b32_e32 v84, 0xffff0000, v192
	v_lshlrev_b32_e32 v94, 16, v194
	v_and_b32_e32 v86, 0xffff0000, v194
	v_mul_f32_e32 v80, v80, v92
	v_mul_f32_e32 v81, v81, v84
	v_mul_f32_e32 v76, v76, v94
	v_mul_f32_e32 v77, v77, v86
	v_mul_f32_e32 v80, 0x41800000, v80
	v_mul_f32_e32 v81, 0x41800000, v81
	v_mul_f32_e32 v76, 0x41800000, v76
	v_mul_f32_e32 v77, 0x41800000, v77
	v_med3_f32 v80, v80, s56, v156
	v_med3_f32 v81, v81, s56, v156
	v_med3_f32 v76, v76, s56, v156
	v_med3_f32 v77, v77, s56, v156
	v_lshlrev_b32_e32 v93, 16, v193
	v_and_b32_e32 v85, 0xffff0000, v193
	v_lshlrev_b32_e32 v95, 16, v195
	v_and_b32_e32 v87, 0xffff0000, v195
	v_cvt_pk_fp8_f32 v90, v80, v81
	v_cvt_pk_fp8_f32 v91, v76, v77
	v_mul_f32_e32 v82, v82, v93
	v_mul_f32_e32 v83, v83, v85
	v_mul_f32_e32 v78, v78, v95
	v_mul_f32_e32 v79, v79, v87
	v_mul_f32_e32 v82, 0x41800000, v82
	v_mul_f32_e32 v83, 0x41800000, v83
	v_mul_f32_e32 v78, 0x41800000, v78
	v_mul_f32_e32 v79, 0x41800000, v79
	v_med3_f32 v82, v82, s56, v156
	v_med3_f32 v83, v83, s56, v156
	v_med3_f32 v76, v78, s56, v156
	v_med3_f32 v77, v79, s56, v156
	v_cvt_pk_fp8_f32 v90, v82, v83 op_sel:[0,0,1]
	v_cvt_pk_fp8_f32 v91, v76, v77 op_sel:[0,0,1]
	v_lshlrev_b64 v[76:77], 11, v[100:101]
	v_lshl_add_u64 v[76:77], s[6:7], 0, v[76:77]
	v_lshl_add_u64 v[80:81], v[76:77], 0, v[144:145]
	global_store_dwordx2 v[80:81], v[90:91], off
	v_mov_b32_e32 v82, 0
	v_mov_b32_e32 v83, 0
	v_add_u32_e32 v84, 0x80, v148
	v_ashrrev_i32_e32 v85, 31, v84
	s_waitcnt vmcnt(15)
	v_lshlrev_b32_e32 v86, 16, v196
	v_and_b32_e32 v76, 0xffff0000, v196
	v_lshlrev_b32_e32 v88, 16, v198
	v_and_b32_e32 v78, 0xffff0000, v198
	v_mul_f32_e32 v72, v72, v86
	v_mul_f32_e32 v73, v73, v76
	v_mul_f32_e32 v68, v68, v88
	v_mul_f32_e32 v69, v69, v78
	v_mul_f32_e32 v72, 0x41800000, v72
	v_mul_f32_e32 v73, 0x41800000, v73
	v_mul_f32_e32 v68, 0x41800000, v68
	v_mul_f32_e32 v69, 0x41800000, v69
	v_med3_f32 v72, v72, s56, v156
	v_med3_f32 v73, v73, s56, v156
	v_med3_f32 v68, v68, s56, v156
	v_med3_f32 v69, v69, s56, v156
	v_lshlrev_b32_e32 v87, 16, v197
	v_and_b32_e32 v77, 0xffff0000, v197
	v_lshlrev_b32_e32 v89, 16, v199
	v_and_b32_e32 v79, 0xffff0000, v199
	v_cvt_pk_fp8_f32 v82, v72, v73
	v_cvt_pk_fp8_f32 v83, v68, v69
	v_mul_f32_e32 v74, v74, v87
	v_mul_f32_e32 v75, v75, v77
	v_mul_f32_e32 v70, v70, v89
	v_mul_f32_e32 v71, v71, v79
	v_mul_f32_e32 v74, 0x41800000, v74
	v_mul_f32_e32 v75, 0x41800000, v75
	v_mul_f32_e32 v70, 0x41800000, v70
	v_mul_f32_e32 v71, 0x41800000, v71
	v_med3_f32 v74, v74, s56, v156
	v_med3_f32 v75, v75, s56, v156
	v_med3_f32 v68, v70, s56, v156
	v_med3_f32 v69, v71, s56, v156
	v_cvt_pk_fp8_f32 v82, v74, v75 op_sel:[0,0,1]
	v_cvt_pk_fp8_f32 v83, v68, v69 op_sel:[0,0,1]
	v_lshlrev_b64 v[68:69], 13, v[84:85]
	v_lshl_add_u64 v[68:69], s[8:9], 0, v[68:69]
	v_lshl_add_u64 v[72:73], v[68:69], 0, v[146:147]
	global_store_dwordx2 v[80:81], v[82:83], off offset:128
	v_mov_b32_e32 v74, 0
	v_mov_b32_e32 v75, 0
	s_waitcnt vmcnt(15)
	v_lshlrev_b32_e32 v76, 16, v200
	v_and_b32_e32 v68, 0xffff0000, v200
	v_lshlrev_b32_e32 v78, 16, v202
	v_and_b32_e32 v70, 0xffff0000, v202
	v_mul_f32_e32 v64, v64, v76
	v_mul_f32_e32 v65, v65, v68
	v_mul_f32_e32 v60, v60, v78
	v_mul_f32_e32 v61, v61, v70
	v_mul_f32_e32 v64, 0x41800000, v64
	v_mul_f32_e32 v65, 0x41800000, v65
	v_mul_f32_e32 v60, 0x41800000, v60
	v_mul_f32_e32 v61, 0x41800000, v61
	v_med3_f32 v64, v64, s56, v156
	v_med3_f32 v65, v65, s56, v156
	v_med3_f32 v60, v60, s56, v156
	v_med3_f32 v61, v61, s56, v156
	v_lshlrev_b32_e32 v77, 16, v201
	v_and_b32_e32 v69, 0xffff0000, v201
	v_lshlrev_b32_e32 v79, 16, v203
	v_and_b32_e32 v71, 0xffff0000, v203
	v_cvt_pk_fp8_f32 v74, v64, v65
	v_cvt_pk_fp8_f32 v75, v60, v61
	v_mul_f32_e32 v66, v66, v77
	v_mul_f32_e32 v67, v67, v69
	v_mul_f32_e32 v62, v62, v79
	v_mul_f32_e32 v63, v63, v71
	v_mul_f32_e32 v66, 0x41800000, v66
	v_mul_f32_e32 v67, 0x41800000, v67
	v_mul_f32_e32 v62, 0x41800000, v62
	v_mul_f32_e32 v63, 0x41800000, v63
	v_med3_f32 v66, v66, s56, v156
	v_med3_f32 v67, v67, s56, v156
	v_med3_f32 v60, v62, s56, v156
	v_med3_f32 v61, v63, s56, v156
	v_cvt_pk_fp8_f32 v74, v66, v67 op_sel:[0,0,1]
	v_cvt_pk_fp8_f32 v75, v60, v61 op_sel:[0,0,1]
	v_lshlrev_b64 v[60:61], 11, v[84:85]
	v_lshl_add_u64 v[60:61], s[6:7], 0, v[60:61]
	v_lshl_add_u64 v[64:65], v[60:61], 0, v[144:145]
	global_store_dwordx2 v[64:65], v[74:75], off
	v_mov_b32_e32 v66, 0
	v_mov_b32_e32 v67, 0
	v_add_u32_e32 v68, 0x90, v148
	v_ashrrev_i32_e32 v69, 31, v68
	s_waitcnt vmcnt(15)
	v_lshlrev_b32_e32 v70, 16, v204
	v_and_b32_e32 v60, 0xffff0000, v204
	v_lshlrev_b32_e32 v72, 16, v206
	v_and_b32_e32 v62, 0xffff0000, v206
	v_mul_f32_e32 v56, v56, v70
	v_mul_f32_e32 v57, v57, v60
	v_mul_f32_e32 v52, v52, v72
	v_mul_f32_e32 v53, v53, v62
	v_mul_f32_e32 v56, 0x41800000, v56
	v_mul_f32_e32 v57, 0x41800000, v57
	v_mul_f32_e32 v52, 0x41800000, v52
	v_mul_f32_e32 v53, 0x41800000, v53
	v_med3_f32 v56, v56, s56, v156
	v_med3_f32 v57, v57, s56, v156
	v_med3_f32 v52, v52, s56, v156
	v_med3_f32 v53, v53, s56, v156
	v_lshlrev_b32_e32 v71, 16, v205
	v_and_b32_e32 v61, 0xffff0000, v205
	v_lshlrev_b32_e32 v73, 16, v207
	v_and_b32_e32 v63, 0xffff0000, v207
	v_cvt_pk_fp8_f32 v66, v56, v57
	v_cvt_pk_fp8_f32 v67, v52, v53
	v_mul_f32_e32 v58, v58, v71
	v_mul_f32_e32 v59, v59, v61
	v_mul_f32_e32 v54, v54, v73
	v_mul_f32_e32 v55, v55, v63
	v_mul_f32_e32 v58, 0x41800000, v58
	v_mul_f32_e32 v59, 0x41800000, v59
	v_mul_f32_e32 v54, 0x41800000, v54
	v_mul_f32_e32 v55, 0x41800000, v55
	v_med3_f32 v58, v58, s56, v156
	v_med3_f32 v59, v59, s56, v156
	v_med3_f32 v52, v54, s56, v156
	v_med3_f32 v53, v55, s56, v156
	v_cvt_pk_fp8_f32 v66, v58, v59 op_sel:[0,0,1]
	v_cvt_pk_fp8_f32 v67, v52, v53 op_sel:[0,0,1]
	v_lshlrev_b64 v[52:53], 13, v[68:69]
	v_lshl_add_u64 v[52:53], s[8:9], 0, v[52:53]
	v_lshl_add_u64 v[56:57], v[52:53], 0, v[146:147]
	global_store_dwordx2 v[64:65], v[66:67], off offset:128
	v_mov_b32_e32 v58, 0
	v_mov_b32_e32 v59, 0
	s_waitcnt vmcnt(15)
	v_lshlrev_b32_e32 v60, 16, v208
	v_and_b32_e32 v52, 0xffff0000, v208
	v_lshlrev_b32_e32 v62, 16, v210
	v_and_b32_e32 v54, 0xffff0000, v210
	v_mul_f32_e32 v48, v48, v60
	v_mul_f32_e32 v49, v49, v52
	v_mul_f32_e32 v44, v44, v62
	v_mul_f32_e32 v45, v45, v54
	v_mul_f32_e32 v48, 0x41800000, v48
	v_mul_f32_e32 v49, 0x41800000, v49
	v_mul_f32_e32 v44, 0x41800000, v44
	v_mul_f32_e32 v45, 0x41800000, v45
	v_med3_f32 v48, v48, s56, v156
	v_med3_f32 v49, v49, s56, v156
	v_med3_f32 v44, v44, s56, v156
	v_med3_f32 v45, v45, s56, v156
	v_lshlrev_b32_e32 v61, 16, v209
	v_and_b32_e32 v53, 0xffff0000, v209
	v_lshlrev_b32_e32 v63, 16, v211
	v_and_b32_e32 v55, 0xffff0000, v211
	v_cvt_pk_fp8_f32 v58, v48, v49
	v_cvt_pk_fp8_f32 v59, v44, v45
	v_mul_f32_e32 v50, v50, v61
	v_mul_f32_e32 v51, v51, v53
	v_mul_f32_e32 v46, v46, v63
	v_mul_f32_e32 v47, v47, v55
	v_mul_f32_e32 v50, 0x41800000, v50
	v_mul_f32_e32 v51, 0x41800000, v51
	v_mul_f32_e32 v46, 0x41800000, v46
	v_mul_f32_e32 v47, 0x41800000, v47
	v_med3_f32 v50, v50, s56, v156
	v_med3_f32 v51, v51, s56, v156
	v_med3_f32 v44, v46, s56, v156
	v_med3_f32 v45, v47, s56, v156
	v_cvt_pk_fp8_f32 v58, v50, v51 op_sel:[0,0,1]
	v_cvt_pk_fp8_f32 v59, v44, v45 op_sel:[0,0,1]
	v_lshlrev_b64 v[44:45], 11, v[68:69]
	v_lshl_add_u64 v[44:45], s[6:7], 0, v[44:45]
	v_lshl_add_u64 v[48:49], v[44:45], 0, v[144:145]
	global_store_dwordx2 v[48:49], v[58:59], off
	v_mov_b32_e32 v50, 0
	v_mov_b32_e32 v51, 0
	v_add_u32_e32 v52, 0xa0, v148
	v_ashrrev_i32_e32 v53, 31, v52
	s_waitcnt vmcnt(15)
	v_lshlrev_b32_e32 v54, 16, v212
	v_and_b32_e32 v44, 0xffff0000, v212
	v_lshlrev_b32_e32 v56, 16, v214
	v_and_b32_e32 v46, 0xffff0000, v214
	v_mul_f32_e32 v40, v40, v54
	v_mul_f32_e32 v41, v41, v44
	v_mul_f32_e32 v36, v36, v56
	v_mul_f32_e32 v37, v37, v46
	v_mul_f32_e32 v40, 0x41800000, v40
	v_mul_f32_e32 v41, 0x41800000, v41
	v_mul_f32_e32 v36, 0x41800000, v36
	v_mul_f32_e32 v37, 0x41800000, v37
	v_med3_f32 v40, v40, s56, v156
	v_med3_f32 v41, v41, s56, v156
	v_med3_f32 v36, v36, s56, v156
	v_med3_f32 v37, v37, s56, v156
	v_lshlrev_b32_e32 v55, 16, v213
	v_and_b32_e32 v45, 0xffff0000, v213
	v_lshlrev_b32_e32 v57, 16, v215
	v_and_b32_e32 v47, 0xffff0000, v215
	v_cvt_pk_fp8_f32 v50, v40, v41
	v_cvt_pk_fp8_f32 v51, v36, v37
	v_mul_f32_e32 v42, v42, v55
	v_mul_f32_e32 v43, v43, v45
	v_mul_f32_e32 v38, v38, v57
	v_mul_f32_e32 v39, v39, v47
	v_mul_f32_e32 v42, 0x41800000, v42
	v_mul_f32_e32 v43, 0x41800000, v43
	v_mul_f32_e32 v38, 0x41800000, v38
	v_mul_f32_e32 v39, 0x41800000, v39
	v_med3_f32 v42, v42, s56, v156
	v_med3_f32 v43, v43, s56, v156
	v_med3_f32 v36, v38, s56, v156
	v_med3_f32 v37, v39, s56, v156
	v_cvt_pk_fp8_f32 v50, v42, v43 op_sel:[0,0,1]
	v_cvt_pk_fp8_f32 v51, v36, v37 op_sel:[0,0,1]
	v_lshlrev_b64 v[36:37], 13, v[52:53]
	v_lshl_add_u64 v[36:37], s[8:9], 0, v[36:37]
	v_lshl_add_u64 v[40:41], v[36:37], 0, v[146:147]
	global_store_dwordx2 v[48:49], v[50:51], off offset:128
	v_mov_b32_e32 v42, 0
	v_mov_b32_e32 v43, 0
	s_waitcnt vmcnt(15)
	v_lshlrev_b32_e32 v44, 16, v216
	v_and_b32_e32 v36, 0xffff0000, v216
	v_lshlrev_b32_e32 v46, 16, v218
	v_and_b32_e32 v38, 0xffff0000, v218
	v_mul_f32_e32 v32, v32, v44
	v_mul_f32_e32 v33, v33, v36
	v_mul_f32_e32 v28, v28, v46
	v_mul_f32_e32 v29, v29, v38
	v_mul_f32_e32 v32, 0x41800000, v32
	v_mul_f32_e32 v33, 0x41800000, v33
	v_mul_f32_e32 v28, 0x41800000, v28
	v_mul_f32_e32 v29, 0x41800000, v29
	v_med3_f32 v32, v32, s56, v156
	v_med3_f32 v33, v33, s56, v156
	v_med3_f32 v28, v28, s56, v156
	v_med3_f32 v29, v29, s56, v156
	v_lshlrev_b32_e32 v45, 16, v217
	v_and_b32_e32 v37, 0xffff0000, v217
	v_lshlrev_b32_e32 v47, 16, v219
	v_and_b32_e32 v39, 0xffff0000, v219
	v_cvt_pk_fp8_f32 v42, v32, v33
	v_cvt_pk_fp8_f32 v43, v28, v29
	v_mul_f32_e32 v34, v34, v45
	v_mul_f32_e32 v35, v35, v37
	v_mul_f32_e32 v30, v30, v47
	v_mul_f32_e32 v31, v31, v39
	v_mul_f32_e32 v34, 0x41800000, v34
	v_mul_f32_e32 v35, 0x41800000, v35
	v_mul_f32_e32 v30, 0x41800000, v30
	v_mul_f32_e32 v31, 0x41800000, v31
	v_med3_f32 v34, v34, s56, v156
	v_med3_f32 v35, v35, s56, v156
	v_med3_f32 v28, v30, s56, v156
	v_med3_f32 v29, v31, s56, v156
	v_cvt_pk_fp8_f32 v42, v34, v35 op_sel:[0,0,1]
	v_cvt_pk_fp8_f32 v43, v28, v29 op_sel:[0,0,1]
	v_lshlrev_b64 v[28:29], 11, v[52:53]
	v_lshl_add_u64 v[28:29], s[6:7], 0, v[28:29]
	v_lshl_add_u64 v[32:33], v[28:29], 0, v[144:145]
	global_store_dwordx2 v[32:33], v[42:43], off
	v_mov_b32_e32 v34, 0
	v_mov_b32_e32 v35, 0
	v_add_u32_e32 v36, 0xb0, v148
	v_ashrrev_i32_e32 v37, 31, v36
	s_waitcnt vmcnt(15)
	v_lshlrev_b32_e32 v38, 16, v220
	v_and_b32_e32 v28, 0xffff0000, v220
	v_lshlrev_b32_e32 v40, 16, v222
	v_and_b32_e32 v30, 0xffff0000, v222
	v_mul_f32_e32 v24, v24, v38
	v_mul_f32_e32 v25, v25, v28
	v_mul_f32_e32 v20, v20, v40
	v_mul_f32_e32 v21, v21, v30
	v_mul_f32_e32 v24, 0x41800000, v24
	v_mul_f32_e32 v25, 0x41800000, v25
	v_mul_f32_e32 v20, 0x41800000, v20
	v_mul_f32_e32 v21, 0x41800000, v21
	v_med3_f32 v24, v24, s56, v156
	v_med3_f32 v25, v25, s56, v156
	v_med3_f32 v20, v20, s56, v156
	v_med3_f32 v21, v21, s56, v156
	v_lshlrev_b32_e32 v39, 16, v221
	v_and_b32_e32 v29, 0xffff0000, v221
	v_lshlrev_b32_e32 v41, 16, v223
	v_and_b32_e32 v31, 0xffff0000, v223
	v_cvt_pk_fp8_f32 v34, v24, v25
	v_cvt_pk_fp8_f32 v35, v20, v21
	v_mul_f32_e32 v26, v26, v39
	v_mul_f32_e32 v27, v27, v29
	v_mul_f32_e32 v22, v22, v41
	v_mul_f32_e32 v23, v23, v31
	v_mul_f32_e32 v26, 0x41800000, v26
	v_mul_f32_e32 v27, 0x41800000, v27
	v_mul_f32_e32 v22, 0x41800000, v22
	v_mul_f32_e32 v23, 0x41800000, v23
	v_med3_f32 v26, v26, s56, v156
	v_med3_f32 v27, v27, s56, v156
	v_med3_f32 v20, v22, s56, v156
	v_med3_f32 v21, v23, s56, v156
	v_cvt_pk_fp8_f32 v34, v26, v27 op_sel:[0,0,1]
	v_cvt_pk_fp8_f32 v35, v20, v21 op_sel:[0,0,1]
	v_lshlrev_b64 v[20:21], 13, v[36:37]
	v_lshl_add_u64 v[20:21], s[8:9], 0, v[20:21]
	v_lshl_add_u64 v[24:25], v[20:21], 0, v[146:147]
	global_store_dwordx2 v[32:33], v[34:35], off offset:128
	v_mov_b32_e32 v26, 0
	v_mov_b32_e32 v27, 0
	s_waitcnt vmcnt(15)
	v_lshlrev_b32_e32 v28, 16, v224
	v_and_b32_e32 v20, 0xffff0000, v224
	v_lshlrev_b32_e32 v30, 16, v226
	v_and_b32_e32 v22, 0xffff0000, v226
	v_mul_f32_e32 v16, v16, v28
	v_mul_f32_e32 v17, v17, v20
	v_mul_f32_e32 v12, v12, v30
	v_mul_f32_e32 v13, v13, v22
	v_mul_f32_e32 v16, 0x41800000, v16
	v_mul_f32_e32 v17, 0x41800000, v17
	v_mul_f32_e32 v12, 0x41800000, v12
	v_mul_f32_e32 v13, 0x41800000, v13
	v_med3_f32 v16, v16, s56, v156
	v_med3_f32 v17, v17, s56, v156
	v_med3_f32 v12, v12, s56, v156
	v_med3_f32 v13, v13, s56, v156
	v_lshlrev_b32_e32 v29, 16, v225
	v_and_b32_e32 v21, 0xffff0000, v225
	v_lshlrev_b32_e32 v31, 16, v227
	v_and_b32_e32 v23, 0xffff0000, v227
	v_cvt_pk_fp8_f32 v26, v16, v17
	v_cvt_pk_fp8_f32 v27, v12, v13
	v_mul_f32_e32 v18, v18, v29
	v_mul_f32_e32 v19, v19, v21
	v_mul_f32_e32 v14, v14, v31
	v_mul_f32_e32 v15, v15, v23
	v_mul_f32_e32 v18, 0x41800000, v18
	v_mul_f32_e32 v19, 0x41800000, v19
	v_mul_f32_e32 v14, 0x41800000, v14
	v_mul_f32_e32 v15, 0x41800000, v15
	v_med3_f32 v18, v18, s56, v156
	v_med3_f32 v19, v19, s56, v156
	v_med3_f32 v12, v14, s56, v156
	v_med3_f32 v13, v15, s56, v156
	v_cvt_pk_fp8_f32 v26, v18, v19 op_sel:[0,0,1]
	v_cvt_pk_fp8_f32 v27, v12, v13 op_sel:[0,0,1]
	v_lshlrev_b64 v[12:13], 11, v[36:37]
	v_lshl_add_u64 v[12:13], s[6:7], 0, v[12:13]
	v_lshl_add_u64 v[16:17], v[12:13], 0, v[144:145]
	global_store_dwordx2 v[16:17], v[26:27], off
	v_mov_b32_e32 v18, 0
	v_mov_b32_e32 v19, 0
	s_waitcnt vmcnt(15)
	v_lshlrev_b32_e32 v20, 16, v228
	v_and_b32_e32 v12, 0xffff0000, v228
	v_lshlrev_b32_e32 v22, 16, v230
	v_and_b32_e32 v14, 0xffff0000, v230
	v_mul_f32_e32 v8, v8, v20
	v_mul_f32_e32 v9, v9, v12
	v_mul_f32_e32 v4, v4, v22
	v_mul_f32_e32 v5, v5, v14
	v_mul_f32_e32 v8, 0x41800000, v8
	v_mul_f32_e32 v9, 0x41800000, v9
	v_mul_f32_e32 v4, 0x41800000, v4
	v_mul_f32_e32 v5, 0x41800000, v5
	v_med3_f32 v8, v8, s56, v156
	v_med3_f32 v9, v9, s56, v156
	v_med3_f32 v4, v4, s56, v156
	v_med3_f32 v5, v5, s56, v156
	v_lshlrev_b32_e32 v21, 16, v229
	v_and_b32_e32 v13, 0xffff0000, v229
	v_lshlrev_b32_e32 v23, 16, v231
	v_and_b32_e32 v15, 0xffff0000, v231
	v_cvt_pk_fp8_f32 v18, v8, v9
	v_cvt_pk_fp8_f32 v19, v4, v5
	v_mul_f32_e32 v10, v10, v21
	v_mul_f32_e32 v11, v11, v13
	v_mul_f32_e32 v6, v6, v23
	v_mul_f32_e32 v7, v7, v15
	v_mul_f32_e32 v10, 0x41800000, v10
	v_mul_f32_e32 v11, 0x41800000, v11
	v_mul_f32_e32 v6, 0x41800000, v6
	v_mul_f32_e32 v7, 0x41800000, v7
	v_med3_f32 v10, v10, s56, v156
	v_med3_f32 v11, v11, s56, v156
	v_med3_f32 v4, v6, s56, v156
	v_med3_f32 v5, v7, s56, v156
	v_cvt_pk_fp8_f32 v18, v10, v11 op_sel:[0,0,1]
	v_cvt_pk_fp8_f32 v19, v4, v5 op_sel:[0,0,1]
	global_store_dwordx2 v[16:17], v[18:19], off offset:128
	s_cbranch_vccnz .LBB0_851
	s_andn2_b64 vcc, exec, s[12:13]
	s_cbranch_vccnz .LBB0_850
	s_barrier
	s_branch .LBB0_850

.LBB0_957:
	s_add_u32 s42, s30, 0x40080
	s_addc_u32 s43, s31, 0
	s_add_u32 s25, s36, 0x100
	s_addc_u32 s27, s37, 0
	s_mov_b32 s38, -2
	ds_read_b128 v[16:19], v185
	ds_read_b128 v[20:23], v185 offset:1024
	ds_read_b128 v[24:27], v185 offset:2048
	ds_read_b128 v[28:31], v185 offset:3072
	ds_read_b128 v[0:3], v186
	ds_read_b128 v[4:7], v186 offset:1024
	ds_read_b128 v[8:11], v186 offset:2048
	ds_read_b128 v[12:15], v186 offset:3072
	s_add_u32 s30, s42, 0xfffc0080
	s_addc_u32 s31, s43, -1
	s_cmp_eq_u32 s38, 12
	s_cselect_b32 s37, s29, s31
	s_cselect_b32 s36, s28, s30
	s_cselect_b32 s31, s35, s27
	s_cselect_b32 s30, s34, s25
	v_lshl_add_u64 v[212:213], s[42:43], 0, v[168:169]
	s_add_i32 m0, s41, 0xc000
	ds_read_b128 v[176:179], v187
	ds_read_b128 v[180:183], v187 offset:1024
	ds_read_b128 v[188:191], v187 offset:2048
	ds_read_b128 v[192:195], v187 offset:3072
	ds_read_b128 v[196:199], v187 offset:4096
	ds_read_b128 v[200:203], v187 offset:5120
	ds_read_b128 v[204:207], v187 offset:6144
	ds_read_b128 v[208:211], v187 offset:7168
	global_load_lds_dwordx4 v[212:213], off
	v_lshl_add_u64 v[212:213], s[42:43], 0, v[170:171]
	s_add_i32 m0, s41, 0xe000
	s_nop 0
	global_load_lds_dwordx4 v[212:213], off
	s_waitcnt vmcnt(8)
	s_waitcnt lgkmcnt(0)
	s_barrier
	s_setprio 1
	s_waitcnt lgkmcnt(0)
	v_mfma_f32_16x16x128_f8f6f4 v[156:159], v[16:23], v[176:183], 0
	v_mfma_f32_16x16x128_f8f6f4 v[152:155], v[24:31], v[176:183], 0
	v_mfma_f32_16x16x128_f8f6f4 v[140:143], v[16:23], v[188:195], 0
	v_mfma_f32_16x16x128_f8f6f4 v[136:139], v[24:31], v[188:195], 0
	v_mfma_f32_16x16x128_f8f6f4 v[124:127], v[16:23], v[196:203], 0
	v_mfma_f32_16x16x128_f8f6f4 v[120:123], v[24:31], v[196:203], 0
	v_mfma_f32_16x16x128_f8f6f4 v[108:111], v[16:23], v[204:211], 0
	v_mfma_f32_16x16x128_f8f6f4 v[104:107], v[24:31], v[204:211], 0
	s_setprio 0
	s_setprio 1
	v_mfma_f32_16x16x128_f8f6f4 v[148:151], v[0:7], v[176:183], 0
	v_mfma_f32_16x16x128_f8f6f4 v[144:147], v[8:15], v[176:183], 0
	v_mfma_f32_16x16x128_f8f6f4 v[132:135], v[0:7], v[188:195], 0
	v_mfma_f32_16x16x128_f8f6f4 v[128:131], v[8:15], v[188:195], 0
	v_mfma_f32_16x16x128_f8f6f4 v[116:119], v[0:7], v[196:203], 0
	v_mfma_f32_16x16x128_f8f6f4 v[112:115], v[8:15], v[196:203], 0
	v_mfma_f32_16x16x128_f8f6f4 v[100:103], v[0:7], v[204:211], 0
	v_mfma_f32_16x16x128_f8f6f4 v[96:99], v[8:15], v[204:211], 0
	s_setprio 0
	s_barrier
	s_add_i32 s39, s57, s47
	v_lshl_add_u64 v[176:177], s[30:31], 0, v[162:163]
	s_mov_b32 m0, s39
	ds_read_b128 v[188:191], v187 offset:16384
	ds_read_b128 v[192:195], v187 offset:17408
	ds_read_b128 v[196:199], v187 offset:18432
	ds_read_b128 v[200:203], v187 offset:19456
	ds_read_b128 v[204:207], v187 offset:20480
	ds_read_b128 v[208:211], v187 offset:21504
	ds_read_b128 v[212:215], v187 offset:22528
	ds_read_b128 v[216:219], v187 offset:23552
	global_load_lds_dwordx4 v[176:177], off
	s_add_i32 m0, s39, 0x2000
	s_add_u32 s60, s30, 0x40000
	v_lshl_add_u64 v[178:179], s[30:31], 0, v[166:167]
	s_addc_u32 s61, s31, 0
	s_add_i32 s39, s58, s47
	global_load_lds_dwordx4 v[178:179], off
	v_lshl_add_u64 v[180:181], s[60:61], 0, v[162:163]
	s_mov_b32 m0, s39
	v_lshl_add_u64 v[182:183], s[36:37], 0, v[164:165]
	global_load_lds_dwordx4 v[180:181], off
	v_lshl_add_u64 v[180:181], s[60:61], 0, v[166:167]
	s_add_i32 m0, s39, 0x2000
	s_nop 0
	global_load_lds_dwordx4 v[180:181], off
	v_lshl_add_u64 v[180:181], s[36:37], 0, v[160:161]
	s_mov_b32 m0, s41
	s_nop 0
	global_load_lds_dwordx4 v[180:181], off
	s_mov_b32 m0, s48
	s_nop 0
	global_load_lds_dwordx4 v[182:183], off
	s_waitcnt vmcnt(8)
	s_waitcnt lgkmcnt(0)
	s_barrier
	s_setprio 1
	s_waitcnt lgkmcnt(0)
	v_mfma_f32_16x16x128_f8f6f4 v[92:95], v[16:23], v[188:195], 0
	v_mfma_f32_16x16x128_f8f6f4 v[88:91], v[24:31], v[188:195], 0
	v_mfma_f32_16x16x128_f8f6f4 v[76:79], v[16:23], v[196:203], 0
	v_mfma_f32_16x16x128_f8f6f4 v[72:75], v[24:31], v[196:203], 0
	v_mfma_f32_16x16x128_f8f6f4 v[60:63], v[16:23], v[204:211], 0
	v_mfma_f32_16x16x128_f8f6f4 v[56:59], v[24:31], v[204:211], 0
	v_mfma_f32_16x16x128_f8f6f4 v[44:47], v[16:23], v[212:219], 0
	v_mfma_f32_16x16x128_f8f6f4 v[40:43], v[24:31], v[212:219], 0
	s_setprio 0
	s_setprio 1
	v_mfma_f32_16x16x128_f8f6f4 v[84:87], v[0:7], v[188:195], 0
	v_mfma_f32_16x16x128_f8f6f4 v[80:83], v[8:15], v[188:195], 0
	v_mfma_f32_16x16x128_f8f6f4 v[68:71], v[0:7], v[196:203], 0
	v_mfma_f32_16x16x128_f8f6f4 v[64:67], v[8:15], v[196:203], 0
	v_mfma_f32_16x16x128_f8f6f4 v[52:55], v[0:7], v[204:211], 0
	v_mfma_f32_16x16x128_f8f6f4 v[48:51], v[8:15], v[204:211], 0
	v_mfma_f32_16x16x128_f8f6f4 v[36:39], v[0:7], v[212:219], 0
	v_mfma_f32_16x16x128_f8f6f4 v[32:35], v[8:15], v[212:219], 0
	s_setprio 0
	s_barrier
	s_branch .Lpeel5_sub3

.Lpeel5_sub3:
	s_add_i32 s39, 0, 0x18000
	s_add_i32 s60, 0, 0x1c000
	v_add_u32_e32 v12, s39, v184
	v_add_u32_e32 v28, s60, v184
	ds_read_b128 v[0:3], v12
	ds_read_b128 v[4:7], v12 offset:1024
	ds_read_b128 v[8:11], v12 offset:2048
	ds_read_b128 v[12:15], v12 offset:3072
	ds_read_b128 v[16:19], v28
	ds_read_b128 v[20:23], v28 offset:1024
	ds_read_b128 v[24:27], v28 offset:2048
	ds_read_b128 v[28:31], v28 offset:3072
	s_add_u32 s36, s36, 0x40000
	s_addc_u32 s37, s37, 0
	s_mov_b32 m0, s49
	v_lshl_add_u64 v[220:221], s[36:37], 0, v[160:161]
	ds_read_b128 v[188:191], v187 offset:32768
	ds_read_b128 v[192:195], v187 offset:33792
	ds_read_b128 v[196:199], v187 offset:34816
	ds_read_b128 v[200:203], v187 offset:35840
	ds_read_b128 v[204:207], v187 offset:36864
	ds_read_b128 v[208:211], v187 offset:37888
	ds_read_b128 v[212:215], v187 offset:38912
	ds_read_b128 v[216:219], v187 offset:39936
	global_load_lds_dwordx4 v[220:221], off
	v_lshl_add_u64 v[220:221], s[36:37], 0, v[164:165]
	s_mov_b32 m0, s50
	s_nop 0
	global_load_lds_dwordx4 v[220:221], off
	s_waitcnt vmcnt(8)
	s_waitcnt lgkmcnt(0)
	s_barrier
	s_setprio 1
	s_waitcnt lgkmcnt(0)
	v_mfma_f32_16x16x128_f8f6f4 v[156:159], v[0:7], v[188:195], v[156:159]
	v_mfma_f32_16x16x128_f8f6f4 v[152:155], v[8:15], v[188:195], v[152:155]
	v_mfma_f32_16x16x128_f8f6f4 v[140:143], v[0:7], v[196:203], v[140:143]
	v_mfma_f32_16x16x128_f8f6f4 v[136:139], v[8:15], v[196:203], v[136:139]
	v_mfma_f32_16x16x128_f8f6f4 v[124:127], v[0:7], v[204:211], v[124:127]
	v_mfma_f32_16x16x128_f8f6f4 v[120:123], v[8:15], v[204:211], v[120:123]
	v_mfma_f32_16x16x128_f8f6f4 v[108:111], v[0:7], v[212:219], v[108:111]
	v_mfma_f32_16x16x128_f8f6f4 v[104:107], v[8:15], v[212:219], v[104:107]
	s_setprio 0
	s_setprio 1
	v_mfma_f32_16x16x128_f8f6f4 v[148:151], v[16:23], v[188:195], v[148:151]
	v_mfma_f32_16x16x128_f8f6f4 v[144:147], v[24:31], v[188:195], v[144:147]
	v_mfma_f32_16x16x128_f8f6f4 v[132:135], v[16:23], v[196:203], v[132:135]
	v_mfma_f32_16x16x128_f8f6f4 v[128:131], v[24:31], v[196:203], v[128:131]
	v_mfma_f32_16x16x128_f8f6f4 v[116:119], v[16:23], v[204:211], v[116:119]
	v_mfma_f32_16x16x128_f8f6f4 v[112:115], v[24:31], v[204:211], v[112:115]
	v_mfma_f32_16x16x128_f8f6f4 v[100:103], v[16:23], v[212:219], v[100:103]
	v_mfma_f32_16x16x128_f8f6f4 v[96:99], v[24:31], v[212:219], v[96:99]
	s_setprio 0
	s_barrier
	s_add_i32 s36, s39, s47
	v_lshl_add_u64 v[176:177], v[176:177], 0, s[10:11]
	s_mov_b32 m0, s36
	ds_read_b128 v[188:191], v187 offset:49152
	ds_read_b128 v[192:195], v187 offset:50176
	ds_read_b128 v[196:199], v187 offset:51200
	ds_read_b128 v[200:203], v187 offset:52224
	ds_read_b128 v[204:207], v187 offset:53248
	ds_read_b128 v[208:211], v187 offset:54272
	ds_read_b128 v[212:215], v187 offset:55296
	ds_read_b128 v[216:219], v187 offset:56320
	global_load_lds_dwordx4 v[176:177], off
	s_add_i32 m0, s36, 0x2000
	s_add_u32 s30, s30, 0x40080
	v_lshl_add_u64 v[176:177], v[178:179], 0, s[10:11]
	s_addc_u32 s31, s31, 0
	s_add_i32 s36, s60, s47
	global_load_lds_dwordx4 v[176:177], off
	v_lshl_add_u64 v[176:177], s[30:31], 0, v[162:163]
	s_mov_b32 m0, s36
	s_nop 0
	global_load_lds_dwordx4 v[176:177], off
	v_lshl_add_u64 v[176:177], s[30:31], 0, v[166:167]
	s_add_i32 m0, s36, 0x2000
	s_nop 0
	global_load_lds_dwordx4 v[176:177], off
	v_lshl_add_u64 v[176:177], v[180:181], 0, s[10:11]
	s_mov_b32 m0, s54
	s_nop 0
	global_load_lds_dwordx4 v[176:177], off
	v_lshl_add_u64 v[176:177], v[182:183], 0, s[10:11]
	s_mov_b32 m0, s55
	s_nop 0
	global_load_lds_dwordx4 v[176:177], off
	s_waitcnt vmcnt(8)
	s_waitcnt lgkmcnt(0)
	s_barrier
	s_setprio 1
	s_waitcnt lgkmcnt(0)
	v_mfma_f32_16x16x128_f8f6f4 v[92:95], v[0:7], v[188:195], v[92:95]
	v_mfma_f32_16x16x128_f8f6f4 v[88:91], v[8:15], v[188:195], v[88:91]
	v_mfma_f32_16x16x128_f8f6f4 v[76:79], v[0:7], v[196:203], v[76:79]
	v_mfma_f32_16x16x128_f8f6f4 v[72:75], v[8:15], v[196:203], v[72:75]
	v_mfma_f32_16x16x128_f8f6f4 v[60:63], v[0:7], v[204:211], v[60:63]
	v_mfma_f32_16x16x128_f8f6f4 v[56:59], v[8:15], v[204:211], v[56:59]
	v_mfma_f32_16x16x128_f8f6f4 v[44:47], v[0:7], v[212:219], v[44:47]
	v_mfma_f32_16x16x128_f8f6f4 v[40:43], v[8:15], v[212:219], v[40:43]
	s_setprio 0
	s_setprio 1
	v_mfma_f32_16x16x128_f8f6f4 v[84:87], v[16:23], v[188:195], v[84:87]
	v_mfma_f32_16x16x128_f8f6f4 v[80:83], v[24:31], v[188:195], v[80:83]
	v_mfma_f32_16x16x128_f8f6f4 v[68:71], v[16:23], v[196:203], v[68:71]
	v_mfma_f32_16x16x128_f8f6f4 v[64:67], v[24:31], v[196:203], v[64:67]
	v_mfma_f32_16x16x128_f8f6f4 v[52:55], v[16:23], v[204:211], v[52:55]
	v_mfma_f32_16x16x128_f8f6f4 v[48:51], v[24:31], v[204:211], v[48:51]
	v_mfma_f32_16x16x128_f8f6f4 v[36:39], v[16:23], v[212:219], v[36:39]
	v_mfma_f32_16x16x128_f8f6f4 v[32:35], v[24:31], v[212:219], v[32:35]
	s_setprio 0
	s_barrier
	s_add_i32 s38, s38, 2
	s_add_u32 s42, s42, 0x100
	s_addc_u32 s43, s43, 0
	s_add_u32 s25, s25, 0x100
	s_addc_u32 s27, s27, 0
	s_cmp_gt_u32 s38, 13
	s_cbranch_scc0 .LBB0_958
	s_and_b64 vcc, exec, s[12:13]
	s_cbranch_vccz .LBB0_961
	s_barrier
.LBB0_961:
	s_lshl_b32 s25, s40, 8
	v_mbcnt_lo_u32_b32 v0, -1, 0
	v_mbcnt_hi_u32_b32 v0, -1, v0
	s_add_i32 s25, s25, s52
	v_and_or_b32 v4, v0, 15, s25
	s_lshl_b32 s25, s59, 8
	v_ashrrev_i32_e32 v0, 1, v0
	s_or_b32 s25, s25, s53
	v_and_b32_e32 v0, -8, v0
	v_add_u32_e32 v2, s25, v0
	v_ashrrev_i32_e32 v5, 31, v4
	v_ashrrev_i32_e32 v3, 31, v2
	v_lshlrev_b64 v[0:1], 11, v[4:5]
	v_lshl_add_u64 v[0:1], v[0:1], 0, v[2:3]
	v_lshlrev_b64 v[0:1], 1, v[0:1]
	v_lshl_add_u64 v[10:11], s[6:7], 0, v[0:1]
	s_mov_b32 s98, 0x10000
	s_mov_b32 s99, 0
	global_load_dwordx4 v[28:31], v[10:11], off
	global_load_dwordx4 v[176:179], v[10:11], off offset:256
	v_lshl_add_u64 v[240:241], v[10:11], 0, s[98:99]
	global_load_dwordx4 v[180:183], v[240:241], off
	global_load_dwordx4 v[188:191], v[240:241], off offset:256
	v_lshl_add_u64 v[240:241], v[240:241], 0, s[98:99]
	global_load_dwordx4 v[192:195], v[240:241], off
	global_load_dwordx4 v[196:199], v[240:241], off offset:256
	v_lshl_add_u64 v[240:241], v[240:241], 0, s[98:99]
	global_load_dwordx4 v[200:203], v[240:241], off
	global_load_dwordx4 v[204:207], v[240:241], off offset:256
	v_lshl_add_u64 v[240:241], v[240:241], 0, s[98:99]
	v_lshl_add_u64 v[240:241], v[240:241], 0, s[98:99]
	v_lshl_add_u64 v[240:241], v[240:241], 0, s[98:99]
	v_lshl_add_u64 v[240:241], v[240:241], 0, s[98:99]
	v_lshl_add_u64 v[240:241], v[240:241], 0, s[98:99]
	global_load_dwordx4 v[208:211], v[240:241], off
	global_load_dwordx4 v[212:215], v[240:241], off offset:256
	v_lshl_add_u64 v[240:241], v[240:241], 0, s[98:99]
	global_load_dwordx4 v[216:219], v[240:241], off
	global_load_dwordx4 v[220:223], v[240:241], off offset:256
	v_lshl_add_u64 v[240:241], v[240:241], 0, s[98:99]
	global_load_dwordx4 v[224:227], v[240:241], off
	global_load_dwordx4 v[228:231], v[240:241], off offset:256
	v_lshl_add_u64 v[240:241], v[240:241], 0, s[98:99]
	global_load_dwordx4 v[232:235], v[240:241], off
	global_load_dwordx4 v[236:239], v[240:241], off offset:256
	v_pk_mul_f32 v[12:13], v[158:159], s[14:15] op_sel_hi:[1,0]
	v_pk_mul_f32 v[14:15], v[156:157], s[14:15] op_sel_hi:[1,0]
	v_pk_mul_f32 v[16:17], v[154:155], s[14:15] op_sel_hi:[1,0]
	v_pk_mul_f32 v[18:19], v[152:153], s[14:15] op_sel_hi:[1,0]
	v_lshl_add_u64 v[24:25], s[8:9], 0, v[0:1]
	s_andn2_b64 vcc, exec, s[0:1]
	s_mov_b64 s[0:1], -1
	s_waitcnt vmcnt(15)
	v_lshlrev_b32_e32 v20, 16, v29
	v_and_b32_e32 v7, 0xffff0000, v29
	v_lshlrev_b32_e32 v5, 16, v28
	v_and_b32_e32 v6, 0xffff0000, v28
	v_lshlrev_b32_e32 v21, 16, v30
	v_and_b32_e32 v8, 0xffff0000, v30
	v_lshlrev_b32_e32 v22, 16, v31
	v_and_b32_e32 v9, 0xffff0000, v31
	v_fmamk_f32 v12, v20, 0x3f9837f0, v12
	v_fmac_f32_e32 v13, 0x3f9837f0, v7
	v_fmamk_f32 v5, v5, 0x3f9837f0, v14
	v_fmac_f32_e32 v15, 0x3f9837f0, v6
	v_fmamk_f32 v14, v21, 0x3f9837f0, v18
	v_fmac_f32_e32 v19, 0x3f9837f0, v8
	v_fmamk_f32 v16, v22, 0x3f9837f0, v16
	v_fmac_f32_e32 v17, 0x3f9837f0, v9
	v_cvt_pk_bf16_f32 v6, v5, v15
	v_cvt_pk_bf16_f32 v7, v12, v13
	v_cvt_pk_bf16_f32 v8, v14, v19
	v_cvt_pk_bf16_f32 v9, v16, v17
	v_or_b32_e32 v22, 16, v4
	v_ashrrev_i32_e32 v23, 31, v22
	v_lshlrev_b64 v[22:23], 11, v[22:23]
	v_pk_mul_f32 v[14:15], v[150:151], s[14:15] op_sel_hi:[1,0]
	v_pk_mul_f32 v[18:19], v[146:147], s[14:15] op_sel_hi:[1,0]
	v_pk_mul_f32 v[20:21], v[144:145], s[14:15] op_sel_hi:[1,0]
	v_lshl_add_u64 v[22:23], v[22:23], 0, v[2:3]
	global_store_dwordx4 v[24:25], v[6:9], off
	v_pk_mul_f32 v[16:17], v[148:149], s[14:15] op_sel_hi:[1,0]
	v_lshlrev_b64 v[22:23], 1, v[22:23]
	v_lshl_add_u64 v[26:27], s[6:7], 0, v[22:23]
	v_lshl_add_u64 v[22:23], s[8:9], 0, v[22:23]
	s_waitcnt vmcnt(15)
	v_lshlrev_b32_e32 v7, 16, v177
	v_and_b32_e32 v8, 0xffff0000, v177
	v_lshlrev_b32_e32 v9, 16, v178
	v_lshlrev_b32_e32 v11, 16, v179
	v_lshlrev_b32_e32 v5, 16, v176
	v_and_b32_e32 v6, 0xffff0000, v176
	v_and_b32_e32 v10, 0xffff0000, v178
	v_and_b32_e32 v12, 0xffff0000, v179
	v_fmamk_f32 v7, v7, 0x3f9837f0, v14
	v_fmac_f32_e32 v15, 0x3f9837f0, v8
	v_fmamk_f32 v8, v9, 0x3f9837f0, v20
	v_fmamk_f32 v9, v11, 0x3f9837f0, v18
	v_fmamk_f32 v5, v5, 0x3f9837f0, v16
	v_fmac_f32_e32 v17, 0x3f9837f0, v6
	v_fmac_f32_e32 v21, 0x3f9837f0, v10
	v_fmac_f32_e32 v19, 0x3f9837f0, v12
	v_cvt_pk_bf16_f32 v6, v5, v17
	v_cvt_pk_bf16_f32 v7, v7, v15
	v_cvt_pk_bf16_f32 v8, v8, v21
	v_cvt_pk_bf16_f32 v9, v9, v19
	global_store_dwordx4 v[24:25], v[6:9], off offset:256
	v_pk_mul_f32 v[10:11], v[142:143], s[14:15] op_sel_hi:[1,0]
	v_pk_mul_f32 v[12:13], v[140:141], s[14:15] op_sel_hi:[1,0]
	v_pk_mul_f32 v[16:17], v[136:137], s[14:15] op_sel_hi:[1,0]
	v_pk_mul_f32 v[14:15], v[138:139], s[14:15] op_sel_hi:[1,0]
	v_or_b32_e32 v24, 32, v4
	v_ashrrev_i32_e32 v25, 31, v24
	v_lshlrev_b64 v[24:25], 11, v[24:25]
	v_lshl_add_u64 v[24:25], v[24:25], 0, v[2:3]
	v_lshlrev_b64 v[24:25], 1, v[24:25]
	v_or_b32_e32 v4, 48, v4
	s_waitcnt vmcnt(15)
	v_lshlrev_b32_e32 v5, 16, v180
	v_and_b32_e32 v6, 0xffff0000, v180
	v_lshlrev_b32_e32 v18, 16, v181
	v_and_b32_e32 v7, 0xffff0000, v181
	v_lshlrev_b32_e32 v19, 16, v182
	v_and_b32_e32 v8, 0xffff0000, v182
	v_lshlrev_b32_e32 v20, 16, v183
	v_and_b32_e32 v9, 0xffff0000, v183
	v_fmamk_f32 v5, v5, 0x3f9837f0, v12
	v_fmac_f32_e32 v13, 0x3f9837f0, v6
	v_fmamk_f32 v10, v18, 0x3f9837f0, v10
	v_fmac_f32_e32 v11, 0x3f9837f0, v7
	v_fmamk_f32 v12, v19, 0x3f9837f0, v16
	v_fmac_f32_e32 v17, 0x3f9837f0, v8
	v_fmamk_f32 v14, v20, 0x3f9837f0, v14
	v_fmac_f32_e32 v15, 0x3f9837f0, v9
	v_cvt_pk_bf16_f32 v6, v5, v13
	v_cvt_pk_bf16_f32 v7, v10, v11
	v_cvt_pk_bf16_f32 v8, v12, v17
	v_cvt_pk_bf16_f32 v9, v14, v15
	v_pk_mul_f32 v[14:15], v[134:135], s[14:15] op_sel_hi:[1,0]
	v_pk_mul_f32 v[18:19], v[130:131], s[14:15] op_sel_hi:[1,0]
	v_pk_mul_f32 v[20:21], v[128:129], s[14:15] op_sel_hi:[1,0]
	global_store_dwordx4 v[22:23], v[6:9], off
	v_pk_mul_f32 v[16:17], v[132:133], s[14:15] op_sel_hi:[1,0]
	v_lshl_add_u64 v[26:27], s[6:7], 0, v[24:25]
	v_lshl_add_u64 v[24:25], s[8:9], 0, v[24:25]
	s_waitcnt vmcnt(15)
	v_lshlrev_b32_e32 v7, 16, v189
	v_and_b32_e32 v8, 0xffff0000, v189
	v_lshlrev_b32_e32 v9, 16, v190
	v_lshlrev_b32_e32 v11, 16, v191
	v_lshlrev_b32_e32 v5, 16, v188
	v_and_b32_e32 v6, 0xffff0000, v188
	v_and_b32_e32 v10, 0xffff0000, v190
	v_and_b32_e32 v12, 0xffff0000, v191
	v_fmamk_f32 v7, v7, 0x3f9837f0, v14
	v_fmac_f32_e32 v15, 0x3f9837f0, v8
	v_fmamk_f32 v8, v9, 0x3f9837f0, v20
	v_fmamk_f32 v9, v11, 0x3f9837f0, v18
	v_fmamk_f32 v5, v5, 0x3f9837f0, v16
	v_fmac_f32_e32 v17, 0x3f9837f0, v6
	v_fmac_f32_e32 v21, 0x3f9837f0, v10
	v_fmac_f32_e32 v19, 0x3f9837f0, v12
	v_cvt_pk_bf16_f32 v6, v5, v17
	v_cvt_pk_bf16_f32 v7, v7, v15
	v_cvt_pk_bf16_f32 v8, v8, v21
	v_cvt_pk_bf16_f32 v9, v9, v19
	global_store_dwordx4 v[22:23], v[6:9], off offset:256
	v_pk_mul_f32 v[10:11], v[126:127], s[14:15] op_sel_hi:[1,0]
	v_pk_mul_f32 v[12:13], v[124:125], s[14:15] op_sel_hi:[1,0]
	v_pk_mul_f32 v[16:17], v[120:121], s[14:15] op_sel_hi:[1,0]
	v_pk_mul_f32 v[14:15], v[122:123], s[14:15] op_sel_hi:[1,0]
	s_waitcnt vmcnt(15)
	v_lshlrev_b32_e32 v5, 16, v192
	v_and_b32_e32 v6, 0xffff0000, v192
	v_lshlrev_b32_e32 v18, 16, v193
	v_and_b32_e32 v7, 0xffff0000, v193
	v_lshlrev_b32_e32 v19, 16, v194
	v_and_b32_e32 v8, 0xffff0000, v194
	v_lshlrev_b32_e32 v20, 16, v195
	v_and_b32_e32 v9, 0xffff0000, v195
	v_fmamk_f32 v5, v5, 0x3f9837f0, v12
	v_fmac_f32_e32 v13, 0x3f9837f0, v6
	v_fmamk_f32 v10, v18, 0x3f9837f0, v10
	v_fmac_f32_e32 v11, 0x3f9837f0, v7
	v_fmamk_f32 v12, v19, 0x3f9837f0, v16
	v_fmac_f32_e32 v17, 0x3f9837f0, v8
	v_fmamk_f32 v14, v20, 0x3f9837f0, v14
	v_fmac_f32_e32 v15, 0x3f9837f0, v9
	v_cvt_pk_bf16_f32 v6, v5, v13
	v_cvt_pk_bf16_f32 v7, v10, v11
	v_cvt_pk_bf16_f32 v8, v12, v17
	v_cvt_pk_bf16_f32 v9, v14, v15
	v_ashrrev_i32_e32 v5, 31, v4
	v_lshlrev_b64 v[4:5], 11, v[4:5]
	v_lshl_add_u64 v[2:3], v[4:5], 0, v[2:3]
	v_pk_mul_f32 v[14:15], v[118:119], s[14:15] op_sel_hi:[1,0]
	v_pk_mul_f32 v[16:17], v[116:117], s[14:15] op_sel_hi:[1,0]
	v_pk_mul_f32 v[18:19], v[114:115], s[14:15] op_sel_hi:[1,0]
	v_pk_mul_f32 v[20:21], v[112:113], s[14:15] op_sel_hi:[1,0]
	v_lshlrev_b64 v[22:23], 1, v[2:3]
	global_store_dwordx4 v[24:25], v[6:9], off
	v_lshl_add_u64 v[26:27], s[6:7], 0, v[22:23]
	s_waitcnt vmcnt(15)
	v_lshlrev_b32_e32 v2, 16, v196
	v_and_b32_e32 v3, 0xffff0000, v196
	v_lshlrev_b32_e32 v4, 16, v197
	v_and_b32_e32 v5, 0xffff0000, v197
	v_lshlrev_b32_e32 v6, 16, v198
	v_lshlrev_b32_e32 v8, 16, v199
	v_and_b32_e32 v7, 0xffff0000, v198
	v_and_b32_e32 v9, 0xffff0000, v199
	v_fmamk_f32 v2, v2, 0x3f9837f0, v16
	v_fmac_f32_e32 v17, 0x3f9837f0, v3
	v_fmamk_f32 v3, v4, 0x3f9837f0, v14
	v_fmac_f32_e32 v15, 0x3f9837f0, v5
	v_fmamk_f32 v4, v6, 0x3f9837f0, v20
	v_fmamk_f32 v5, v8, 0x3f9837f0, v18
	v_fmac_f32_e32 v21, 0x3f9837f0, v7
	v_fmac_f32_e32 v19, 0x3f9837f0, v9
	v_cvt_pk_bf16_f32 v2, v2, v17
	v_cvt_pk_bf16_f32 v3, v3, v15
	v_cvt_pk_bf16_f32 v4, v4, v21
	v_cvt_pk_bf16_f32 v5, v5, v19
	global_store_dwordx4 v[24:25], v[2:5], off offset:256
	v_pk_mul_f32 v[6:7], v[110:111], s[14:15] op_sel_hi:[1,0]
	v_pk_mul_f32 v[8:9], v[108:109], s[14:15] op_sel_hi:[1,0]
	v_pk_mul_f32 v[10:11], v[106:107], s[14:15] op_sel_hi:[1,0]
	v_pk_mul_f32 v[12:13], v[104:105], s[14:15] op_sel_hi:[1,0]
	v_lshl_add_u64 v[20:21], s[8:9], 0, v[22:23]
	v_lshl_add_u64 v[18:19], v[0:1], 0, s[16:17]
	v_lshl_add_u64 v[22:23], s[6:7], 0, v[18:19]
	v_lshl_add_u64 v[18:19], s[8:9], 0, v[18:19]
	s_waitcnt vmcnt(15)
	v_lshlrev_b32_e32 v14, 16, v200
	v_and_b32_e32 v2, 0xffff0000, v200
	v_lshlrev_b32_e32 v15, 16, v201
	v_and_b32_e32 v3, 0xffff0000, v201
	v_lshlrev_b32_e32 v16, 16, v202
	v_and_b32_e32 v4, 0xffff0000, v202
	v_lshlrev_b32_e32 v17, 16, v203
	v_and_b32_e32 v5, 0xffff0000, v203
	v_fmamk_f32 v8, v14, 0x3f9837f0, v8
	v_fmac_f32_e32 v9, 0x3f9837f0, v2
	v_fmamk_f32 v6, v15, 0x3f9837f0, v6
	v_fmac_f32_e32 v7, 0x3f9837f0, v3
	v_fmamk_f32 v12, v16, 0x3f9837f0, v12
	v_fmac_f32_e32 v13, 0x3f9837f0, v4
	v_fmamk_f32 v10, v17, 0x3f9837f0, v10
	v_fmac_f32_e32 v11, 0x3f9837f0, v5
	v_cvt_pk_bf16_f32 v2, v8, v9
	v_cvt_pk_bf16_f32 v3, v6, v7
	v_cvt_pk_bf16_f32 v4, v12, v13
	v_cvt_pk_bf16_f32 v5, v10, v11
	v_pk_mul_f32 v[10:11], v[102:103], s[14:15] op_sel_hi:[1,0]
	v_pk_mul_f32 v[12:13], v[100:101], s[14:15] op_sel_hi:[1,0]
	v_pk_mul_f32 v[14:15], v[98:99], s[14:15] op_sel_hi:[1,0]
	v_pk_mul_f32 v[16:17], v[96:97], s[14:15] op_sel_hi:[1,0]
	global_store_dwordx4 v[20:21], v[2:5], off
	s_nop 0
	s_waitcnt vmcnt(15)
	v_lshlrev_b32_e32 v2, 16, v204
	v_and_b32_e32 v3, 0xffff0000, v204
	v_lshlrev_b32_e32 v4, 16, v205
	v_and_b32_e32 v5, 0xffff0000, v205
	v_lshlrev_b32_e32 v6, 16, v206
	v_and_b32_e32 v7, 0xffff0000, v206
	v_lshlrev_b32_e32 v8, 16, v207
	v_and_b32_e32 v9, 0xffff0000, v207
	v_fmamk_f32 v2, v2, 0x3f9837f0, v12
	v_fmac_f32_e32 v13, 0x3f9837f0, v3
	v_fmamk_f32 v3, v4, 0x3f9837f0, v10
	v_fmac_f32_e32 v11, 0x3f9837f0, v5
	v_fmamk_f32 v4, v6, 0x3f9837f0, v16
	v_fmamk_f32 v5, v8, 0x3f9837f0, v14
	v_fmac_f32_e32 v17, 0x3f9837f0, v7
	v_fmac_f32_e32 v15, 0x3f9837f0, v9
	v_cvt_pk_bf16_f32 v2, v2, v13
	v_cvt_pk_bf16_f32 v3, v3, v11
	v_cvt_pk_bf16_f32 v4, v4, v17
	v_cvt_pk_bf16_f32 v5, v5, v15
	global_store_dwordx4 v[20:21], v[2:5], off offset:256
	v_pk_mul_f32 v[6:7], v[94:95], s[14:15] op_sel_hi:[1,0]
	v_pk_mul_f32 v[8:9], v[92:93], s[14:15] op_sel_hi:[1,0]
	v_pk_mul_f32 v[10:11], v[90:91], s[14:15] op_sel_hi:[1,0]
	v_pk_mul_f32 v[12:13], v[88:89], s[14:15] op_sel_hi:[1,0]
	v_lshl_add_u64 v[20:21], v[0:1], 0, s[18:19]
	s_waitcnt vmcnt(15)
	v_lshlrev_b32_e32 v14, 16, v208
	v_and_b32_e32 v2, 0xffff0000, v208
	v_lshlrev_b32_e32 v15, 16, v209
	v_and_b32_e32 v3, 0xffff0000, v209
	v_lshlrev_b32_e32 v16, 16, v210
	v_and_b32_e32 v4, 0xffff0000, v210
	v_lshlrev_b32_e32 v17, 16, v211
	v_and_b32_e32 v5, 0xffff0000, v211
	v_fmamk_f32 v8, v14, 0x3f9837f0, v8
	v_fmac_f32_e32 v9, 0x3f9837f0, v2
	v_fmamk_f32 v6, v15, 0x3f9837f0, v6
	v_fmac_f32_e32 v7, 0x3f9837f0, v3
	v_fmamk_f32 v12, v16, 0x3f9837f0, v12
	v_fmac_f32_e32 v13, 0x3f9837f0, v4
	v_fmamk_f32 v10, v17, 0x3f9837f0, v10
	v_fmac_f32_e32 v11, 0x3f9837f0, v5
	v_cvt_pk_bf16_f32 v2, v8, v9
	v_cvt_pk_bf16_f32 v3, v6, v7
	v_cvt_pk_bf16_f32 v4, v12, v13
	v_cvt_pk_bf16_f32 v5, v10, v11
	v_pk_mul_f32 v[10:11], v[86:87], s[14:15] op_sel_hi:[1,0]
	v_pk_mul_f32 v[12:13], v[84:85], s[14:15] op_sel_hi:[1,0]
	v_pk_mul_f32 v[14:15], v[82:83], s[14:15] op_sel_hi:[1,0]
	v_pk_mul_f32 v[16:17], v[80:81], s[14:15] op_sel_hi:[1,0]
	global_store_dwordx4 v[18:19], v[2:5], off
	v_lshl_add_u64 v[22:23], s[6:7], 0, v[20:21]
	v_lshl_add_u64 v[20:21], s[8:9], 0, v[20:21]
	s_waitcnt vmcnt(15)
	v_lshlrev_b32_e32 v2, 16, v212
	v_and_b32_e32 v3, 0xffff0000, v212
	v_lshlrev_b32_e32 v4, 16, v213
	v_and_b32_e32 v5, 0xffff0000, v213
	v_lshlrev_b32_e32 v6, 16, v214
	v_and_b32_e32 v7, 0xffff0000, v214
	v_lshlrev_b32_e32 v8, 16, v215
	v_and_b32_e32 v9, 0xffff0000, v215
	v_fmamk_f32 v2, v2, 0x3f9837f0, v12
	v_fmac_f32_e32 v13, 0x3f9837f0, v3
	v_fmamk_f32 v3, v4, 0x3f9837f0, v10
	v_fmac_f32_e32 v11, 0x3f9837f0, v5
	v_fmamk_f32 v4, v6, 0x3f9837f0, v16
	v_fmamk_f32 v5, v8, 0x3f9837f0, v14
	v_fmac_f32_e32 v17, 0x3f9837f0, v7
	v_fmac_f32_e32 v15, 0x3f9837f0, v9
	v_cvt_pk_bf16_f32 v2, v2, v13
	v_cvt_pk_bf16_f32 v3, v3, v11
	v_cvt_pk_bf16_f32 v4, v4, v17
	v_cvt_pk_bf16_f32 v5, v5, v15
	global_store_dwordx4 v[18:19], v[2:5], off offset:256
	v_pk_mul_f32 v[6:7], v[78:79], s[14:15] op_sel_hi:[1,0]
	v_pk_mul_f32 v[8:9], v[76:77], s[14:15] op_sel_hi:[1,0]
	v_pk_mul_f32 v[10:11], v[74:75], s[14:15] op_sel_hi:[1,0]
	v_pk_mul_f32 v[12:13], v[72:73], s[14:15] op_sel_hi:[1,0]
	v_lshl_add_u64 v[18:19], v[0:1], 0, s[20:21]
	s_waitcnt vmcnt(15)
	v_lshlrev_b32_e32 v14, 16, v216
	v_and_b32_e32 v2, 0xffff0000, v216
	v_lshlrev_b32_e32 v15, 16, v217
	v_and_b32_e32 v3, 0xffff0000, v217
	v_lshlrev_b32_e32 v16, 16, v218
	v_and_b32_e32 v4, 0xffff0000, v218
	v_lshlrev_b32_e32 v17, 16, v219
	v_and_b32_e32 v5, 0xffff0000, v219
	v_fmamk_f32 v8, v14, 0x3f9837f0, v8
	v_fmac_f32_e32 v9, 0x3f9837f0, v2
	v_fmamk_f32 v6, v15, 0x3f9837f0, v6
	v_fmac_f32_e32 v7, 0x3f9837f0, v3
	v_fmamk_f32 v12, v16, 0x3f9837f0, v12
	v_fmac_f32_e32 v13, 0x3f9837f0, v4
	v_fmamk_f32 v10, v17, 0x3f9837f0, v10
	v_fmac_f32_e32 v11, 0x3f9837f0, v5
	v_cvt_pk_bf16_f32 v2, v8, v9
	v_cvt_pk_bf16_f32 v3, v6, v7
	v_cvt_pk_bf16_f32 v4, v12, v13
	v_cvt_pk_bf16_f32 v5, v10, v11
	v_pk_mul_f32 v[10:11], v[70:71], s[14:15] op_sel_hi:[1,0]
	v_pk_mul_f32 v[12:13], v[68:69], s[14:15] op_sel_hi:[1,0]
	v_pk_mul_f32 v[14:15], v[66:67], s[14:15] op_sel_hi:[1,0]
	v_pk_mul_f32 v[16:17], v[64:65], s[14:15] op_sel_hi:[1,0]
	global_store_dwordx4 v[20:21], v[2:5], off
	v_lshl_add_u64 v[22:23], s[6:7], 0, v[18:19]
	v_lshl_add_u64 v[18:19], s[8:9], 0, v[18:19]
	s_waitcnt vmcnt(15)
	v_lshlrev_b32_e32 v2, 16, v220
	v_and_b32_e32 v3, 0xffff0000, v220
	v_lshlrev_b32_e32 v4, 16, v221
	v_and_b32_e32 v5, 0xffff0000, v221
	v_lshlrev_b32_e32 v6, 16, v222
	v_and_b32_e32 v7, 0xffff0000, v222
	v_lshlrev_b32_e32 v8, 16, v223
	v_and_b32_e32 v9, 0xffff0000, v223
	v_fmamk_f32 v2, v2, 0x3f9837f0, v12
	v_fmac_f32_e32 v13, 0x3f9837f0, v3
	v_fmamk_f32 v3, v4, 0x3f9837f0, v10
	v_fmac_f32_e32 v11, 0x3f9837f0, v5
	v_fmamk_f32 v4, v6, 0x3f9837f0, v16
	v_fmamk_f32 v5, v8, 0x3f9837f0, v14
	v_fmac_f32_e32 v17, 0x3f9837f0, v7
	v_fmac_f32_e32 v15, 0x3f9837f0, v9
	v_cvt_pk_bf16_f32 v2, v2, v13
	v_cvt_pk_bf16_f32 v3, v3, v11
	v_cvt_pk_bf16_f32 v4, v4, v17
	v_cvt_pk_bf16_f32 v5, v5, v15
	global_store_dwordx4 v[20:21], v[2:5], off offset:256
	v_pk_mul_f32 v[6:7], v[62:63], s[14:15] op_sel_hi:[1,0]
	v_pk_mul_f32 v[8:9], v[60:61], s[14:15] op_sel_hi:[1,0]
	v_pk_mul_f32 v[10:11], v[58:59], s[14:15] op_sel_hi:[1,0]
	v_pk_mul_f32 v[12:13], v[56:57], s[14:15] op_sel_hi:[1,0]
	v_lshl_add_u64 v[20:21], v[0:1], 0, s[22:23]
	s_waitcnt vmcnt(15)
	v_lshlrev_b32_e32 v14, 16, v224
	v_and_b32_e32 v2, 0xffff0000, v224
	v_lshlrev_b32_e32 v15, 16, v225
	v_and_b32_e32 v3, 0xffff0000, v225
	v_lshlrev_b32_e32 v16, 16, v226
	v_and_b32_e32 v4, 0xffff0000, v226
	v_lshlrev_b32_e32 v17, 16, v227
	v_and_b32_e32 v5, 0xffff0000, v227
	v_fmamk_f32 v8, v14, 0x3f9837f0, v8
	v_fmac_f32_e32 v9, 0x3f9837f0, v2
	v_fmamk_f32 v6, v15, 0x3f9837f0, v6
	v_fmac_f32_e32 v7, 0x3f9837f0, v3
	v_fmamk_f32 v12, v16, 0x3f9837f0, v12
	v_fmac_f32_e32 v13, 0x3f9837f0, v4
	v_fmamk_f32 v10, v17, 0x3f9837f0, v10
	v_fmac_f32_e32 v11, 0x3f9837f0, v5
	v_cvt_pk_bf16_f32 v2, v8, v9
	v_cvt_pk_bf16_f32 v3, v6, v7
	v_cvt_pk_bf16_f32 v4, v12, v13
	v_cvt_pk_bf16_f32 v5, v10, v11
	v_pk_mul_f32 v[10:11], v[54:55], s[14:15] op_sel_hi:[1,0]
	v_pk_mul_f32 v[12:13], v[52:53], s[14:15] op_sel_hi:[1,0]
	v_pk_mul_f32 v[14:15], v[50:51], s[14:15] op_sel_hi:[1,0]
	v_pk_mul_f32 v[16:17], v[48:49], s[14:15] op_sel_hi:[1,0]
	global_store_dwordx4 v[18:19], v[2:5], off
	v_lshl_add_u64 v[22:23], s[6:7], 0, v[20:21]
	s_waitcnt vmcnt(15)
	v_lshlrev_b32_e32 v0, 16, v228
	v_and_b32_e32 v1, 0xffff0000, v228
	v_lshlrev_b32_e32 v2, 16, v229
	v_and_b32_e32 v3, 0xffff0000, v229
	v_lshlrev_b32_e32 v4, 16, v230
	v_lshlrev_b32_e32 v6, 16, v231
	v_and_b32_e32 v5, 0xffff0000, v230
	v_and_b32_e32 v7, 0xffff0000, v231
	v_fmamk_f32 v0, v0, 0x3f9837f0, v12
	v_fmac_f32_e32 v13, 0x3f9837f0, v1
	v_fmamk_f32 v1, v2, 0x3f9837f0, v10
	v_fmac_f32_e32 v11, 0x3f9837f0, v3
	v_fmamk_f32 v2, v4, 0x3f9837f0, v16
	v_fmamk_f32 v3, v6, 0x3f9837f0, v14
	v_fmac_f32_e32 v17, 0x3f9837f0, v5
	v_fmac_f32_e32 v15, 0x3f9837f0, v7
	v_cvt_pk_bf16_f32 v0, v0, v13
	v_cvt_pk_bf16_f32 v1, v1, v11
	v_cvt_pk_bf16_f32 v2, v2, v17
	v_cvt_pk_bf16_f32 v3, v3, v15
	global_store_dwordx4 v[18:19], v[0:3], off offset:256
	v_pk_mul_f32 v[4:5], v[46:47], s[14:15] op_sel_hi:[1,0]
	v_pk_mul_f32 v[6:7], v[44:45], s[14:15] op_sel_hi:[1,0]
	v_pk_mul_f32 v[8:9], v[42:43], s[14:15] op_sel_hi:[1,0]
	v_pk_mul_f32 v[10:11], v[40:41], s[14:15] op_sel_hi:[1,0]
	v_lshl_add_u64 v[16:17], s[8:9], 0, v[20:21]
	s_waitcnt vmcnt(15)
	v_lshlrev_b32_e32 v12, 16, v232
	v_and_b32_e32 v0, 0xffff0000, v232
	v_lshlrev_b32_e32 v13, 16, v233
	v_and_b32_e32 v1, 0xffff0000, v233
	v_lshlrev_b32_e32 v14, 16, v234
	v_and_b32_e32 v2, 0xffff0000, v234
	v_lshlrev_b32_e32 v15, 16, v235
	v_and_b32_e32 v3, 0xffff0000, v235
	v_fmamk_f32 v6, v12, 0x3f9837f0, v6
	v_fmac_f32_e32 v7, 0x3f9837f0, v0
	v_fmamk_f32 v4, v13, 0x3f9837f0, v4
	v_fmac_f32_e32 v5, 0x3f9837f0, v1
	v_fmamk_f32 v10, v14, 0x3f9837f0, v10
	v_fmac_f32_e32 v11, 0x3f9837f0, v2
	v_fmamk_f32 v8, v15, 0x3f9837f0, v8
	v_fmac_f32_e32 v9, 0x3f9837f0, v3
	v_cvt_pk_bf16_f32 v0, v6, v7
	v_cvt_pk_bf16_f32 v1, v4, v5
	v_cvt_pk_bf16_f32 v2, v10, v11
	v_cvt_pk_bf16_f32 v3, v8, v9
	v_pk_mul_f32 v[8:9], v[38:39], s[14:15] op_sel_hi:[1,0]
	v_pk_mul_f32 v[10:11], v[36:37], s[14:15] op_sel_hi:[1,0]
	v_pk_mul_f32 v[12:13], v[34:35], s[14:15] op_sel_hi:[1,0]
	v_pk_mul_f32 v[14:15], v[32:33], s[14:15] op_sel_hi:[1,0]
	global_store_dwordx4 v[16:17], v[0:3], off
	s_nop 0
	s_waitcnt vmcnt(15)
	v_lshlrev_b32_e32 v0, 16, v236
	v_and_b32_e32 v1, 0xffff0000, v236
	v_lshlrev_b32_e32 v2, 16, v237
	v_and_b32_e32 v3, 0xffff0000, v237
	v_lshlrev_b32_e32 v4, 16, v238
	v_and_b32_e32 v5, 0xffff0000, v238
	v_lshlrev_b32_e32 v6, 16, v239
	v_and_b32_e32 v7, 0xffff0000, v239
	v_fmamk_f32 v0, v0, 0x3f9837f0, v10
	v_fmac_f32_e32 v11, 0x3f9837f0, v1
	v_fmamk_f32 v1, v2, 0x3f9837f0, v8
	v_fmac_f32_e32 v9, 0x3f9837f0, v3
	v_fmamk_f32 v2, v4, 0x3f9837f0, v14
	v_fmamk_f32 v3, v6, 0x3f9837f0, v12
	v_fmac_f32_e32 v15, 0x3f9837f0, v5
	v_fmac_f32_e32 v13, 0x3f9837f0, v7
	v_cvt_pk_bf16_f32 v0, v0, v11
	v_cvt_pk_bf16_f32 v1, v1, v9
	v_cvt_pk_bf16_f32 v2, v2, v15
	v_cvt_pk_bf16_f32 v3, v3, v13
	global_store_dwordx4 v[16:17], v[0:3], off offset:256
	s_cbranch_vccnz .LBB0_950
	s_andn2_b64 vcc, exec, s[4:5]
	s_cbranch_vccnz .LBB0_949
	s_barrier
	s_branch .LBB0_949

.LBB0_1269:
	s_ashr_i32 s43, s42, 31
	v_readlane_b32 s80, v251, 2
	s_lshl_b64 s[44:45], s[42:43], 13
	s_lshl_b32 s42, s34, 8
	s_lshl_b32 s34, s30, 8
	v_readlane_b32 s82, v251, 4
	v_readlane_b32 s83, v251, 5
	s_ashr_i32 s43, s42, 31
	s_ashr_i32 s35, s34, 31
	s_mov_b64 s[78:79], s[82:83]
	s_add_u32 s21, s78, s44
	s_addc_u32 s23, s79, s45
	s_lshl_b64 s[30:31], s[42:43], 2
	s_add_u32 s21, s21, s30
	s_addc_u32 s23, s23, s31
	s_add_u32 s21, s21, s18
	s_addc_u32 s23, s23, s19
	s_lshl_b64 s[30:31], s[34:35], 2
	s_add_u32 s35, s7, s30
	s_addc_u32 s43, s69, s31
	s_and_b64 s[30:31], s[16:17], exec
	s_cselect_b32 s23, s43, s23
	s_cselect_b32 s21, s35, s21
	s_add_u32 s44, s36, 0x40080
	s_addc_u32 s45, s37, 0
	v_mov_b32_e32 v0, s21
	v_mov_b32_e32 v1, s23
	s_add_u32 s21, s38, 0x100
	v_lshl_add_u64 v[176:177], v[160:161], 2, v[0:1]
	s_addc_u32 s23, s39, 0
	s_mov_b32 s35, -2
	v_readlane_b32 s81, v251, 3
	v_readlane_b32 s84, v251, 6
	v_readlane_b32 s85, v251, 7
	v_readlane_b32 s86, v251, 8
	v_readlane_b32 s87, v251, 9
	s_branch .Lpeel9_hdr

.Lpeel9_cont:
	v_add_u32_e32 v0, s74, v186
	v_add_u32_e32 v12, s75, v186
	ds_read_b128 v[16:19], v0
	ds_read_b128 v[20:23], v0 offset:1024
	ds_read_b128 v[24:27], v0 offset:2048
	ds_read_b128 v[28:31], v0 offset:3072
	ds_read_b128 v[0:3], v12
	ds_read_b128 v[4:7], v12 offset:1024
	ds_read_b128 v[8:11], v12 offset:2048
	ds_read_b128 v[12:15], v12 offset:3072
	s_add_u32 s36, s44, 0xfffc0080
	s_addc_u32 s37, s45, -1
	s_and_b64 s[30:31], s[30:31], exec
	s_cselect_b32 s37, s29, s37
	s_cselect_b32 s36, s28, s36
	s_cselect_b32 s31, s41, s23
	s_cselect_b32 s30, s40, s21
	v_lshl_add_u64 v[214:215], s[44:45], 0, v[170:171]
	s_add_i32 m0, s62, 0xc000
	ds_read_b128 v[178:181], v187
	ds_read_b128 v[182:185], v187 offset:1024
	ds_read_b128 v[190:193], v187 offset:2048
	ds_read_b128 v[194:197], v187 offset:3072
	ds_read_b128 v[198:201], v187 offset:4096
	ds_read_b128 v[202:205], v187 offset:5120
	ds_read_b128 v[206:209], v187 offset:6144
	ds_read_b128 v[210:213], v187 offset:7168
	global_load_lds_dwordx4 v[214:215], off
	v_lshl_add_u64 v[214:215], s[44:45], 0, v[172:173]
	s_add_i32 m0, s62, 0xe000
	s_nop 0
	global_load_lds_dwordx4 v[214:215], off
	s_waitcnt vmcnt(8)
	s_waitcnt lgkmcnt(0)
	s_barrier
	s_setprio 1
	s_waitcnt lgkmcnt(0)
	v_mfma_f32_16x16x128_f8f6f4 v[156:159], v[16:23], v[178:185], 0
	v_mfma_f32_16x16x128_f8f6f4 v[152:155], v[24:31], v[178:185], 0
	v_mfma_f32_16x16x128_f8f6f4 v[140:143], v[16:23], v[190:197], 0
	v_mfma_f32_16x16x128_f8f6f4 v[136:139], v[24:31], v[190:197], 0
	v_mfma_f32_16x16x128_f8f6f4 v[124:127], v[16:23], v[198:205], 0
	v_mfma_f32_16x16x128_f8f6f4 v[120:123], v[24:31], v[198:205], 0
	v_mfma_f32_16x16x128_f8f6f4 v[108:111], v[16:23], v[206:213], 0
	v_mfma_f32_16x16x128_f8f6f4 v[104:107], v[24:31], v[206:213], 0
	s_setprio 0
	s_setprio 1
	v_mfma_f32_16x16x128_f8f6f4 v[148:151], v[0:7], v[178:185], 0
	v_mfma_f32_16x16x128_f8f6f4 v[144:147], v[8:15], v[178:185], 0
	v_mfma_f32_16x16x128_f8f6f4 v[132:135], v[0:7], v[190:197], 0
	v_mfma_f32_16x16x128_f8f6f4 v[128:131], v[8:15], v[190:197], 0
	v_mfma_f32_16x16x128_f8f6f4 v[116:119], v[0:7], v[198:205], 0
	v_mfma_f32_16x16x128_f8f6f4 v[112:115], v[8:15], v[198:205], 0
	v_mfma_f32_16x16x128_f8f6f4 v[100:103], v[0:7], v[206:213], 0
	v_mfma_f32_16x16x128_f8f6f4 v[96:99], v[8:15], v[206:213], 0
	s_setprio 0
	s_barrier
	s_add_i32 s38, s74, s47
	v_lshl_add_u64 v[178:179], s[30:31], 0, v[164:165]
	s_mov_b32 m0, s38
	ds_read_b128 v[190:193], v187 offset:16384
	ds_read_b128 v[194:197], v187 offset:17408
	ds_read_b128 v[198:201], v187 offset:18432
	ds_read_b128 v[202:205], v187 offset:19456
	ds_read_b128 v[206:209], v187 offset:20480
	ds_read_b128 v[210:213], v187 offset:21504
	ds_read_b128 v[214:217], v187 offset:22528
	ds_read_b128 v[218:221], v187 offset:23552
	global_load_lds_dwordx4 v[178:179], off
	s_add_i32 m0, s38, 0x2000
	s_add_u32 s38, s30, 0x40000
	v_lshl_add_u64 v[180:181], s[30:31], 0, v[168:169]
	s_addc_u32 s39, s31, 0
	s_add_i32 s43, s75, s47
	global_load_lds_dwordx4 v[180:181], off
	v_lshl_add_u64 v[182:183], s[38:39], 0, v[164:165]
	s_mov_b32 m0, s43
	v_lshl_add_u64 v[184:185], s[36:37], 0, v[166:167]
	global_load_lds_dwordx4 v[182:183], off
	v_lshl_add_u64 v[182:183], s[38:39], 0, v[168:169]
	s_add_i32 m0, s43, 0x2000
	s_nop 0
	global_load_lds_dwordx4 v[182:183], off
	v_lshl_add_u64 v[182:183], s[36:37], 0, v[162:163]
	s_mov_b32 m0, s62
	s_nop 0
	global_load_lds_dwordx4 v[182:183], off
	s_mov_b32 m0, s63
	s_nop 0
	global_load_lds_dwordx4 v[184:185], off
	s_waitcnt vmcnt(8)
	s_waitcnt lgkmcnt(0)
	s_barrier
	s_setprio 1
	s_waitcnt lgkmcnt(0)
	v_mfma_f32_16x16x128_f8f6f4 v[92:95], v[16:23], v[190:197], 0
	v_mfma_f32_16x16x128_f8f6f4 v[88:91], v[24:31], v[190:197], 0
	v_mfma_f32_16x16x128_f8f6f4 v[76:79], v[16:23], v[198:205], 0
	v_mfma_f32_16x16x128_f8f6f4 v[72:75], v[24:31], v[198:205], 0
	v_mfma_f32_16x16x128_f8f6f4 v[60:63], v[16:23], v[206:213], 0
	v_mfma_f32_16x16x128_f8f6f4 v[56:59], v[24:31], v[206:213], 0
	v_mfma_f32_16x16x128_f8f6f4 v[44:47], v[16:23], v[214:221], 0
	v_mfma_f32_16x16x128_f8f6f4 v[40:43], v[24:31], v[214:221], 0
	s_setprio 0
	s_setprio 1
	v_mfma_f32_16x16x128_f8f6f4 v[84:87], v[0:7], v[190:197], 0
	v_mfma_f32_16x16x128_f8f6f4 v[80:83], v[8:15], v[190:197], 0
	v_mfma_f32_16x16x128_f8f6f4 v[68:71], v[0:7], v[198:205], 0
	v_mfma_f32_16x16x128_f8f6f4 v[64:67], v[8:15], v[198:205], 0
	v_mfma_f32_16x16x128_f8f6f4 v[52:55], v[0:7], v[206:213], 0
	v_mfma_f32_16x16x128_f8f6f4 v[48:51], v[8:15], v[206:213], 0
	v_mfma_f32_16x16x128_f8f6f4 v[36:39], v[0:7], v[214:221], 0
	v_mfma_f32_16x16x128_f8f6f4 v[32:35], v[8:15], v[214:221], 0
	s_setprio 0
	s_barrier
	s_branch .Lpeel9_sub3

.Lpeel9_sub3:
	s_add_i32 s38, 0, 0x18000
	s_add_i32 s39, 0, 0x1c000
	v_add_u32_e32 v12, s38, v186
	v_add_u32_e32 v28, s39, v186
	ds_read_b128 v[0:3], v12
	ds_read_b128 v[4:7], v12 offset:1024
	ds_read_b128 v[8:11], v12 offset:2048
	ds_read_b128 v[12:15], v12 offset:3072
	ds_read_b128 v[16:19], v28
	ds_read_b128 v[20:23], v28 offset:1024
	ds_read_b128 v[24:27], v28 offset:2048
	ds_read_b128 v[28:31], v28 offset:3072
	s_add_u32 s36, s36, 0x40000
	s_addc_u32 s37, s37, 0
	s_mov_b32 m0, s64
	v_lshl_add_u64 v[222:223], s[36:37], 0, v[162:163]
	ds_read_b128 v[190:193], v187 offset:32768
	ds_read_b128 v[194:197], v187 offset:33792
	ds_read_b128 v[198:201], v187 offset:34816
	ds_read_b128 v[202:205], v187 offset:35840
	ds_read_b128 v[206:209], v187 offset:36864
	ds_read_b128 v[210:213], v187 offset:37888
	ds_read_b128 v[214:217], v187 offset:38912
	ds_read_b128 v[218:221], v187 offset:39936
	global_load_lds_dwordx4 v[222:223], off
	v_lshl_add_u64 v[222:223], s[36:37], 0, v[166:167]
	s_mov_b32 m0, s65
	s_nop 0
	global_load_lds_dwordx4 v[222:223], off
	s_waitcnt vmcnt(8)
	s_waitcnt lgkmcnt(0)
	s_barrier
	s_setprio 1
	s_waitcnt lgkmcnt(0)
	v_mfma_f32_16x16x128_f8f6f4 v[156:159], v[0:7], v[190:197], v[156:159]
	v_mfma_f32_16x16x128_f8f6f4 v[152:155], v[8:15], v[190:197], v[152:155]
	v_mfma_f32_16x16x128_f8f6f4 v[140:143], v[0:7], v[198:205], v[140:143]
	v_mfma_f32_16x16x128_f8f6f4 v[136:139], v[8:15], v[198:205], v[136:139]
	v_mfma_f32_16x16x128_f8f6f4 v[124:127], v[0:7], v[206:213], v[124:127]
	v_mfma_f32_16x16x128_f8f6f4 v[120:123], v[8:15], v[206:213], v[120:123]
	v_mfma_f32_16x16x128_f8f6f4 v[108:111], v[0:7], v[214:221], v[108:111]
	v_mfma_f32_16x16x128_f8f6f4 v[104:107], v[8:15], v[214:221], v[104:107]
	s_setprio 0
	s_setprio 1
	v_mfma_f32_16x16x128_f8f6f4 v[148:151], v[16:23], v[190:197], v[148:151]
	v_mfma_f32_16x16x128_f8f6f4 v[144:147], v[24:31], v[190:197], v[144:147]
	v_mfma_f32_16x16x128_f8f6f4 v[132:135], v[16:23], v[198:205], v[132:135]
	v_mfma_f32_16x16x128_f8f6f4 v[128:131], v[24:31], v[198:205], v[128:131]
	v_mfma_f32_16x16x128_f8f6f4 v[116:119], v[16:23], v[206:213], v[116:119]
	v_mfma_f32_16x16x128_f8f6f4 v[112:115], v[24:31], v[206:213], v[112:115]
	v_mfma_f32_16x16x128_f8f6f4 v[100:103], v[16:23], v[214:221], v[100:103]
	v_mfma_f32_16x16x128_f8f6f4 v[96:99], v[24:31], v[214:221], v[96:99]
	s_setprio 0
	s_barrier
	s_add_i32 s36, s38, s47
	v_lshl_add_u64 v[178:179], v[178:179], 0, s[14:15]
	s_mov_b32 m0, s36
	ds_read_b128 v[190:193], v187 offset:49152
	ds_read_b128 v[194:197], v187 offset:50176
	ds_read_b128 v[198:201], v187 offset:51200
	ds_read_b128 v[202:205], v187 offset:52224
	ds_read_b128 v[206:209], v187 offset:53248
	ds_read_b128 v[210:213], v187 offset:54272
	ds_read_b128 v[214:217], v187 offset:55296
	ds_read_b128 v[218:221], v187 offset:56320
	global_load_lds_dwordx4 v[178:179], off
	s_add_i32 m0, s36, 0x2000
	s_add_u32 s30, s30, 0x40080
	v_lshl_add_u64 v[178:179], v[180:181], 0, s[14:15]
	s_addc_u32 s31, s31, 0
	s_add_i32 s36, s39, s47
	global_load_lds_dwordx4 v[178:179], off
	v_lshl_add_u64 v[178:179], s[30:31], 0, v[164:165]
	s_mov_b32 m0, s36
	s_nop 0
	global_load_lds_dwordx4 v[178:179], off
	v_lshl_add_u64 v[178:179], s[30:31], 0, v[168:169]
	s_add_i32 m0, s36, 0x2000
	s_nop 0
	global_load_lds_dwordx4 v[178:179], off
	v_lshl_add_u64 v[178:179], v[182:183], 0, s[14:15]
	s_mov_b32 m0, s66
	s_nop 0
	global_load_lds_dwordx4 v[178:179], off
	v_lshl_add_u64 v[178:179], v[184:185], 0, s[14:15]
	s_mov_b32 m0, s67
	s_nop 0
	global_load_lds_dwordx4 v[178:179], off
	s_waitcnt vmcnt(8)
	s_waitcnt lgkmcnt(0)
	s_barrier
	s_setprio 1
	s_waitcnt lgkmcnt(0)
	v_mfma_f32_16x16x128_f8f6f4 v[92:95], v[0:7], v[190:197], v[92:95]
	v_mfma_f32_16x16x128_f8f6f4 v[88:91], v[8:15], v[190:197], v[88:91]
	v_mfma_f32_16x16x128_f8f6f4 v[76:79], v[0:7], v[198:205], v[76:79]
	v_mfma_f32_16x16x128_f8f6f4 v[72:75], v[8:15], v[198:205], v[72:75]
	v_mfma_f32_16x16x128_f8f6f4 v[60:63], v[0:7], v[206:213], v[60:63]
	v_mfma_f32_16x16x128_f8f6f4 v[56:59], v[8:15], v[206:213], v[56:59]
	v_mfma_f32_16x16x128_f8f6f4 v[44:47], v[0:7], v[214:221], v[44:47]
	v_mfma_f32_16x16x128_f8f6f4 v[40:43], v[8:15], v[214:221], v[40:43]
	s_setprio 0
	s_setprio 1
	v_mfma_f32_16x16x128_f8f6f4 v[84:87], v[16:23], v[190:197], v[84:87]
	v_mfma_f32_16x16x128_f8f6f4 v[80:83], v[24:31], v[190:197], v[80:83]
	v_mfma_f32_16x16x128_f8f6f4 v[68:71], v[16:23], v[198:205], v[68:71]
	v_mfma_f32_16x16x128_f8f6f4 v[64:67], v[24:31], v[198:205], v[64:67]
	v_mfma_f32_16x16x128_f8f6f4 v[52:55], v[16:23], v[206:213], v[52:55]
	v_mfma_f32_16x16x128_f8f6f4 v[48:51], v[24:31], v[206:213], v[48:51]
	v_mfma_f32_16x16x128_f8f6f4 v[36:39], v[16:23], v[214:221], v[36:39]
	v_mfma_f32_16x16x128_f8f6f4 v[32:35], v[24:31], v[214:221], v[32:35]
	s_setprio 0
	s_barrier
	s_add_i32 s35, s35, 2
	s_add_u32 s44, s44, 0x100
	s_addc_u32 s45, s45, 0
	s_add_u32 s21, s21, 0x100
	s_addc_u32 s23, s23, 0
	s_cmp_gt_u32 s35, 13
	s_cbranch_scc1 .LBB0_1273

	.amdhsa_kernel _Z6mk_fwd4Args
		.amdhsa_group_segment_fixed_size 0
		.amdhsa_private_segment_fixed_size 0
		.amdhsa_kernarg_size 440
		.amdhsa_user_sgpr_count 2
		.amdhsa_user_sgpr_dispatch_ptr 0
		.amdhsa_user_sgpr_queue_ptr 0
		.amdhsa_user_sgpr_kernarg_segment_ptr 1
		.amdhsa_user_sgpr_dispatch_id 0
		.amdhsa_user_sgpr_kernarg_preload_length 0
		.amdhsa_user_sgpr_kernarg_preload_offset 0
		.amdhsa_user_sgpr_private_segment_size 0
		.amdhsa_uses_dynamic_stack 0
		.amdhsa_enable_private_segment 0
		.amdhsa_system_sgpr_workgroup_id_x 1
		.amdhsa_system_sgpr_workgroup_id_y 0
		.amdhsa_system_sgpr_workgroup_id_z 0
		.amdhsa_system_sgpr_workgroup_info 0
		.amdhsa_system_vgpr_workitem_id 0
		.amdhsa_next_free_vgpr 252
		.amdhsa_next_free_sgpr 102
		.amdhsa_accum_offset 252
		.amdhsa_reserve_vcc 1
		.amdhsa_float_round_mode_32 0
		.amdhsa_float_round_mode_16_64 0
		.amdhsa_float_denorm_mode_32 3
		.amdhsa_float_denorm_mode_16_64 3
		.amdhsa_dx10_clamp 1
		.amdhsa_ieee_mode 1
		.amdhsa_fp16_overflow 0
		.amdhsa_tg_split 0
		.amdhsa_exception_fp_ieee_invalid_op 0
		.amdhsa_exception_fp_denorm_src 0
		.amdhsa_exception_fp_ieee_div_zero 0
		.amdhsa_exception_fp_ieee_overflow 0
		.amdhsa_exception_fp_ieee_underflow 0
		.amdhsa_exception_fp_ieee_inexact 0
		.amdhsa_exception_int_div_zero 0
	.end_amdhsa_kernel

amdhsa.kernels:
  - .agpr_count:     0
    .args:
      - .offset:         0
        .size:           184
        .value_kind:     by_value
      - .offset:         184
        .size:           4
        .value_kind:     hidden_block_count_x
      - .offset:         188
        .size:           4
        .value_kind:     hidden_block_count_y
      - .offset:         192
        .size:           4
        .value_kind:     hidden_block_count_z
      - .offset:         196
        .size:           2
        .value_kind:     hidden_group_size_x
      - .offset:         198
        .size:           2
        .value_kind:     hidden_group_size_y
      - .offset:         200
        .size:           2
        .value_kind:     hidden_group_size_z
      - .offset:         202
        .size:           2
        .value_kind:     hidden_remainder_x
      - .offset:         204
        .size:           2
        .value_kind:     hidden_remainder_y
      - .offset:         206
        .size:           2
        .value_kind:     hidden_remainder_z
      - .offset:         224
        .size:           8
        .value_kind:     hidden_global_offset_x
      - .offset:         232
        .size:           8
        .value_kind:     hidden_global_offset_y
      - .offset:         240
        .size:           8
        .value_kind:     hidden_global_offset_z
      - .offset:         248
        .size:           2
        .value_kind:     hidden_grid_dims
      - .offset:         304
        .size:           4
        .value_kind:     hidden_dynamic_lds_size
    .group_segment_fixed_size: 0
    .kernarg_segment_align: 8
    .kernarg_segment_size: 440
    .language:       OpenCL C
    .language_version:
      - 2
      - 0
    .max_flat_workgroup_size: 512
    .name:           _Z6mk_fwd4Args
    .private_segment_fixed_size: 0
    .sgpr_count:     108
    .sgpr_spill_count: 210
    .symbol:         _Z6mk_fwd4Args.kd
    .uniform_work_group_size: 1
    .uses_dynamic_stack: false
    .vgpr_count:     252
    .vgpr_spill_count: 0
    .wavefront_size: 64
